# speedup vs baseline: 1.0130x; 1.0014x over previous
.LBB3_35:
	s_andn2_b64 vcc, exec, s[2:3]
	s_cbranch_vccnz .LBB3_39
	s_waitcnt vmcnt(4)
	v_ashrrev_i32_e32 v81, 31, v80
	v_lshl_add_u64 v[2:3], v[80:81], 3, s[20:21]
	v_add_co_u32_e32 v2, vcc, 0x48000, v2
	s_movk_i32 s8, 0x620
	s_nop 0
	v_addc_co_u32_e32 v3, vcc, 0, v3, vcc
	global_load_dwordx2 v[82:83], v[2:3], off
	v_and_b32_e32 v2, 0x70, v7
	v_bitop3_b32 v2, v0, v2, 48 bitop3:0x6c
	s_waitcnt vmcnt(4)
	v_mad_u64_u32 v[64:65], s[6:7], v9, s8, v[2:3]
	v_lshrrev_b32_e32 v3, 4, v92
	v_bitop3_b32 v3, v3, v0, 4 bitop3:0x36
	v_lshlrev_b32_e32 v3, 4, v3
	v_and_b32_e32 v4, 0x70, v3
	s_waitcnt vmcnt(3)
	v_mad_u64_u32 v[66:67], s[6:7], v8, s8, v[4:5]
	s_waitcnt vmcnt(2)
	v_mad_u64_u32 v[68:69], s[6:7], v6, s8, v[2:3]
	s_waitcnt vmcnt(1)
	v_mad_u64_u32 v[70:71], s[6:7], v1, s8, v[4:5]
	v_lshrrev_b32_e32 v85, 5, v92
	v_bfe_u32 v2, v0, 1, 3
	s_mov_b64 s[6:7], 0x1800
	s_add_u32 s4, s20, 0x4000000
	v_bitop3_b32 v32, v85, v2, 2 bitop3:0x36
	v_bitop3_b32 v33, v85, v2, 4 bitop3:0x36
	v_bitop3_b32 v34, v85, v2, 6 bitop3:0x36
	v_lshl_add_u64 v[2:3], v[86:87], 0, s[6:7]
	s_addc_u32 s5, s21, 0
	s_lshl_b32 s2, s27, 12
	s_addk_i32 s2, 0x6000
	v_lshrrev_b32_e32 v1, 1, v0
	v_or_b32_e32 v81, s2, v84
	v_lshlrev_b32_e32 v0, 7, v0
	v_and_b32_e32 v8, 0xf80, v0
	v_lshlrev_b32_e32 v9, 4, v32
	v_bitop3_b32 v1, v85, v1, 7 bitop3:0x78
	v_or3_b32 v96, s2, v9, v8
	v_lshlrev_b32_e32 v9, 4, v33
	v_lshlrev_b32_e32 v1, 4, v1
	v_or3_b32 v97, s2, v9, v8
	v_lshlrev_b32_e32 v9, 4, v34
	v_or3_b32 v95, s2, v1, v8
	v_or3_b32 v94, s2, v9, v8
	v_add_u32_e32 v98, 0x103c0, v84
	global_load_dwordx4 v[116:119], v64, s[4:5] offset:0
	global_load_dwordx4 v[120:123], v66, s[4:5] offset:0
	global_load_dwordx4 v[124:127], v68, s[4:5] offset:0
	global_load_dwordx4 v[128:131], v70, s[4:5] offset:0
	global_load_dwordx4 v[132:135], v64, s[4:5] offset:128
	global_load_dwordx4 v[136:139], v66, s[4:5] offset:128
	global_load_dwordx4 v[140:143], v68, s[4:5] offset:128
	global_load_dwordx4 v[144:147], v70, s[4:5] offset:128
	global_load_dwordx4 v[148:151], v64, s[4:5] offset:256
	global_load_dwordx4 v[152:155], v66, s[4:5] offset:256
	global_load_dwordx4 v[156:159], v68, s[4:5] offset:256
	global_load_dwordx4 v[72:75], v70, s[4:5] offset:256
	s_add_u32 m0, s46, 0x0
	s_nop 0
	global_load_lds_dwordx4 v76, s[40:41]
	s_add_u32 m0, s47, 0x0
	s_nop 0
	global_load_lds_dwordx4 v77, s[42:43]
	s_add_u32 m0, s48, 0x0
	s_nop 0
	global_load_lds_dwordx4 v78, s[44:45]
	s_add_u32 m0, s46, 0x3000
	s_add_u32 s40, s40, 0x1800
	s_addc_u32 s41, s41, 0
	global_load_lds_dwordx4 v76, s[40:41]
	s_add_u32 m0, s47, 0x3000
	s_add_u32 s42, s42, 0x1800
	s_addc_u32 s43, s43, 0
	global_load_lds_dwordx4 v77, s[42:43]
	s_add_u32 m0, s48, 0x3000
	s_add_u32 s44, s44, 0x1800
	s_addc_u32 s45, s45, 0
	global_load_lds_dwordx4 v78, s[44:45]
	s_add_u32 m0, s46, 0xd3c0
	s_add_u32 s40, s40, 0x1800
	s_addc_u32 s41, s41, 0
	global_load_lds_dwordx4 v76, s[40:41]
	s_add_u32 m0, s47, 0xd3c0
	s_add_u32 s42, s42, 0x1800
	s_addc_u32 s43, s43, 0
	global_load_lds_dwordx4 v77, s[42:43]
	s_add_u32 m0, s48, 0xd3c0
	s_add_u32 s44, s44, 0x1800
	s_addc_u32 s45, s45, 0
	global_load_lds_dwordx4 v78, s[44:45]
	s_add_u32 m0, s46, 0x103c0
	s_add_u32 s40, s40, 0x1800
	s_addc_u32 s41, s41, 0
	global_load_lds_dwordx4 v76, s[40:41]
	s_add_u32 m0, s47, 0x103c0
	s_add_u32 s42, s42, 0x1800
	s_addc_u32 s43, s43, 0
	global_load_lds_dwordx4 v77, s[42:43]
	s_add_u32 m0, s48, 0x103c0
	s_add_u32 s44, s44, 0x1800
	s_addc_u32 s45, s45, 0
	global_load_lds_dwordx4 v78, s[44:45]
	s_waitcnt vmcnt(20)
	ds_write_b128 v81, v[116:119]
	ds_write_b128 v81, v[120:123] offset:1024
	ds_write_b128 v81, v[124:127] offset:2048
	ds_write_b128 v81, v[128:131] offset:3072
	ds_read_b128 v[52:55], v95
	ds_read_b128 v[56:59], v96
	ds_read_b128 v[60:63], v97
	ds_read_b128 v[0:3], v94
	global_load_dwordx4 v[116:119], v64, s[4:5] offset:384
	global_load_dwordx4 v[120:123], v66, s[4:5] offset:384
	global_load_dwordx4 v[124:127], v68, s[4:5] offset:384
	global_load_dwordx4 v[128:131], v70, s[4:5] offset:384
	s_waitcnt vmcnt(13)
	s_waitcnt lgkmcnt(0)
	s_barrier
	ds_read_b128 v[4:7], v84 offset:0
	ds_read_b128 v[8:11], v84 offset:1024
	ds_read_b128 v[12:15], v84 offset:2048
	ds_read_b128 v[16:19], v84 offset:3072
	ds_read_b128 v[20:23], v84 offset:4096
	ds_read_b128 v[24:27], v84 offset:5120
	ds_read_b128 v[28:31], v84 offset:6144
	ds_read_b128 v[32:35], v84 offset:7168
	ds_read_b128 v[36:39], v84 offset:8192
	ds_read_b128 v[40:43], v84 offset:9216
	ds_read_b128 v[44:47], v84 offset:10240
	ds_read_b128 v[48:51], v84 offset:11264
	s_waitcnt lgkmcnt(6)
	v_mfma_f32_32x32x16_f16 a[80:95], v[4:7], v[52:55], 0
	v_mfma_f32_32x32x16_f16 a[64:79], v[8:11], v[52:55], 0
	v_mfma_f32_32x32x16_f16 a[48:63], v[12:15], v[52:55], 0
	s_waitcnt vmcnt(10)
	s_waitcnt lgkmcnt(0)
	s_barrier
	ds_read_b128 v[4:7], v84 offset:12288
	ds_read_b128 v[8:11], v84 offset:13312
	ds_read_b128 v[12:15], v84 offset:14336
	v_mfma_f32_32x32x16_f16 a[32:47], v[16:19], v[52:55], 0
	ds_read_b128 v[16:19], v84 offset:15360
	v_mfma_f32_32x32x16_f16 a[16:31], v[20:23], v[52:55], 0
	ds_read_b128 v[20:23], v84 offset:16384
	v_mfma_f32_32x32x16_f16 a[0:15], v[24:27], v[52:55], 0
	ds_read_b128 v[24:27], v84 offset:17408
	v_mfma_f32_32x32x16_f16 a[80:95], v[28:31], v[56:59], a[80:95]
	s_add_u32 m0, s46, 0x0
	s_add_u32 s40, s40, 0x1800
	s_addc_u32 s41, s41, 0
	global_load_lds_dwordx4 v76, s[40:41]
	ds_read_b128 v[28:31], v84 offset:18432
	v_mfma_f32_32x32x16_f16 a[64:79], v[32:35], v[56:59], a[64:79]
	ds_read_b128 v[32:35], v84 offset:19456
	v_mfma_f32_32x32x16_f16 a[48:63], v[36:39], v[56:59], a[48:63]
	s_add_u32 m0, s47, 0x0
	s_add_u32 s42, s42, 0x1800
	s_addc_u32 s43, s43, 0
	global_load_lds_dwordx4 v77, s[42:43]
	ds_read_b128 v[36:39], v84 offset:20480
	v_mfma_f32_32x32x16_f16 a[32:47], v[40:43], v[56:59], a[32:47]
	ds_read_b128 v[40:43], v84 offset:21504
	v_mfma_f32_32x32x16_f16 a[16:31], v[44:47], v[56:59], a[16:31]
	s_add_u32 m0, s48, 0x0
	s_add_u32 s44, s44, 0x1800
	s_addc_u32 s45, s45, 0
	global_load_lds_dwordx4 v78, s[44:45]
	ds_read_b128 v[44:47], v84 offset:22528
	v_mfma_f32_32x32x16_f16 a[0:15], v[48:51], v[56:59], a[0:15]
	ds_read_b128 v[48:51], v84 offset:23552
	s_waitcnt lgkmcnt(6)
	v_mfma_f32_32x32x16_f16 a[80:95], v[4:7], v[60:63], a[80:95]
	s_waitcnt vmcnt(23)
	ds_write_b128 v81, v[132:135]
	ds_write_b128 v81, v[136:139] offset:1024
	v_mfma_f32_32x32x16_f16 a[64:79], v[8:11], v[60:63], a[64:79]
	ds_write_b128 v81, v[140:143] offset:2048
	ds_write_b128 v81, v[144:147] offset:3072
	v_mfma_f32_32x32x16_f16 a[48:63], v[12:15], v[60:63], a[48:63]
	ds_read_b128 v[100:103], v95
	ds_read_b128 v[104:107], v96
	ds_read_b128 v[108:111], v97
	ds_read_b128 v[112:115], v94
	s_waitcnt vmcnt(10)
	s_waitcnt lgkmcnt(8)
	s_barrier
	ds_read_b128 v[4:7], v84 offset:54208
	ds_read_b128 v[8:11], v84 offset:55232
	ds_read_b128 v[12:15], v84 offset:56256
	v_mfma_f32_32x32x16_f16 a[32:47], v[16:19], v[60:63], a[32:47]
	ds_read_b128 v[16:19], v84 offset:57280
	v_mfma_f32_32x32x16_f16 a[16:31], v[20:23], v[60:63], a[16:31]
	ds_read_b128 v[20:23], v84 offset:58304
	v_mfma_f32_32x32x16_f16 a[0:15], v[24:27], v[60:63], a[0:15]
	ds_read_b128 v[24:27], v84 offset:59328
	s_waitcnt lgkmcnt(6)
	v_mfma_f32_32x32x16_f16 a[80:95], v[28:31], v[0:3], a[80:95]
	s_add_u32 m0, s46, 0x3000
	s_add_u32 s40, s40, 0x1800
	s_addc_u32 s41, s41, 0
	global_load_lds_dwordx4 v76, s[40:41]
	ds_read_b128 v[28:31], v84 offset:60352
	v_mfma_f32_32x32x16_f16 a[64:79], v[32:35], v[0:3], a[64:79]
	global_load_dwordx4 v[132:135], v64, s[4:5] offset:512
	global_load_dwordx4 v[136:139], v66, s[4:5] offset:512
	ds_read_b128 v[32:35], v84 offset:61376
	v_mfma_f32_32x32x16_f16 a[48:63], v[36:39], v[0:3], a[48:63]
	s_add_u32 m0, s47, 0x3000
	s_add_u32 s42, s42, 0x1800
	s_addc_u32 s43, s43, 0
	global_load_lds_dwordx4 v77, s[42:43]
	ds_read_b128 v[36:39], v84 offset:62400
	v_mfma_f32_32x32x16_f16 a[32:47], v[40:43], v[0:3], a[32:47]
	global_load_dwordx4 v[140:143], v68, s[4:5] offset:512
	global_load_dwordx4 v[144:147], v70, s[4:5] offset:512
	ds_read_b128 v[40:43], v84 offset:63424
	v_mfma_f32_32x32x16_f16 a[16:31], v[44:47], v[0:3], a[16:31]
	s_add_u32 m0, s48, 0x3000
	s_add_u32 s44, s44, 0x1800
	s_addc_u32 s45, s45, 0
	global_load_lds_dwordx4 v78, s[44:45]
	ds_read_b128 v[44:47], v84 offset:64448
	v_mfma_f32_32x32x16_f16 a[0:15], v[48:51], v[0:3], a[0:15]
	ds_read_b128 v[48:51], v84 offset:65472
	s_waitcnt lgkmcnt(6)
	v_mfma_f32_32x32x16_f16 a[80:95], v[4:7], v[100:103], a[80:95]
	v_mfma_f32_32x32x16_f16 a[64:79], v[8:11], v[100:103], a[64:79]
	v_mfma_f32_32x32x16_f16 a[48:63], v[12:15], v[100:103], a[48:63]
	s_waitcnt vmcnt(14)
	s_waitcnt lgkmcnt(0)
	s_barrier
	ds_read_b128 v[4:7], v98
	ds_read_b128 v[8:11], v98 offset:1024
	ds_read_b128 v[12:15], v98 offset:2048
	v_mfma_f32_32x32x16_f16 a[32:47], v[16:19], v[100:103], a[32:47]
	ds_read_b128 v[16:19], v98 offset:3072
	v_mfma_f32_32x32x16_f16 a[16:31], v[20:23], v[100:103], a[16:31]
	ds_read_b128 v[20:23], v98 offset:4096
	v_mfma_f32_32x32x16_f16 a[0:15], v[24:27], v[100:103], a[0:15]
	ds_read_b128 v[24:27], v98 offset:5120
	v_mfma_f32_32x32x16_f16 a[80:95], v[28:31], v[104:107], a[80:95]
	s_add_u32 m0, s46, 0xd3c0
	s_add_u32 s40, s40, 0x1800
	s_addc_u32 s41, s41, 0
	global_load_lds_dwordx4 v76, s[40:41]
	ds_read_b128 v[28:31], v98 offset:6144
	v_mfma_f32_32x32x16_f16 a[64:79], v[32:35], v[104:107], a[64:79]
	ds_read_b128 v[32:35], v98 offset:7168
	v_mfma_f32_32x32x16_f16 a[48:63], v[36:39], v[104:107], a[48:63]
	s_add_u32 m0, s47, 0xd3c0
	s_add_u32 s42, s42, 0x1800
	s_addc_u32 s43, s43, 0
	global_load_lds_dwordx4 v77, s[42:43]
	ds_read_b128 v[36:39], v98 offset:8192
	v_mfma_f32_32x32x16_f16 a[32:47], v[40:43], v[104:107], a[32:47]
	ds_read_b128 v[40:43], v98 offset:9216
	v_mfma_f32_32x32x16_f16 a[16:31], v[44:47], v[104:107], a[16:31]
	s_add_u32 m0, s48, 0xd3c0
	s_add_u32 s44, s44, 0x1800
	s_addc_u32 s45, s45, 0
	global_load_lds_dwordx4 v78, s[44:45]
	ds_read_b128 v[44:47], v98 offset:10240
	v_mfma_f32_32x32x16_f16 a[0:15], v[48:51], v[104:107], a[0:15]
	ds_read_b128 v[48:51], v98 offset:11264
	s_waitcnt lgkmcnt(6)
	v_mfma_f32_32x32x16_f16 a[80:95], v[4:7], v[108:111], a[80:95]
	s_waitcnt vmcnt(29)
	ds_write_b128 v81, v[148:151]
	ds_write_b128 v81, v[152:155] offset:1024
	v_mfma_f32_32x32x16_f16 a[64:79], v[8:11], v[108:111], a[64:79]
	ds_write_b128 v81, v[156:159] offset:2048
	ds_write_b128 v81, v[72:75] offset:3072
	v_mfma_f32_32x32x16_f16 a[48:63], v[12:15], v[108:111], a[48:63]
	ds_read_b128 v[52:55], v95
	ds_read_b128 v[56:59], v96
	ds_read_b128 v[60:63], v97
	ds_read_b128 v[0:3], v94
	s_waitcnt vmcnt(10)
	s_waitcnt lgkmcnt(8)
	s_barrier
	ds_read_b128 v[4:7], v84 offset:0
	ds_read_b128 v[8:11], v84 offset:1024
	ds_read_b128 v[12:15], v84 offset:2048
	v_mfma_f32_32x32x16_f16 a[32:47], v[16:19], v[108:111], a[32:47]
	ds_read_b128 v[16:19], v84 offset:3072
	v_mfma_f32_32x32x16_f16 a[16:31], v[20:23], v[108:111], a[16:31]
	ds_read_b128 v[20:23], v84 offset:4096
	v_mfma_f32_32x32x16_f16 a[0:15], v[24:27], v[108:111], a[0:15]
	ds_read_b128 v[24:27], v84 offset:5120
	s_waitcnt lgkmcnt(6)
	v_mfma_f32_32x32x16_f16 a[80:95], v[28:31], v[112:115], a[80:95]
	s_add_u32 m0, s46, 0x103c0
	s_add_u32 s40, s40, 0x1800
	s_addc_u32 s41, s41, 0
	global_load_lds_dwordx4 v76, s[40:41]
	ds_read_b128 v[28:31], v84 offset:6144
	v_mfma_f32_32x32x16_f16 a[64:79], v[32:35], v[112:115], a[64:79]
	global_load_dwordx4 v[148:151], v64, s[4:5] offset:640
	global_load_dwordx4 v[152:155], v66, s[4:5] offset:640
	ds_read_b128 v[32:35], v84 offset:7168
	v_mfma_f32_32x32x16_f16 a[48:63], v[36:39], v[112:115], a[48:63]
	s_add_u32 m0, s47, 0x103c0
	s_add_u32 s42, s42, 0x1800
	s_addc_u32 s43, s43, 0
	global_load_lds_dwordx4 v77, s[42:43]
	ds_read_b128 v[36:39], v84 offset:8192
	v_mfma_f32_32x32x16_f16 a[32:47], v[40:43], v[112:115], a[32:47]
	global_load_dwordx4 v[156:159], v68, s[4:5] offset:640
	global_load_dwordx4 v[72:75], v70, s[4:5] offset:640
	ds_read_b128 v[40:43], v84 offset:9216
	v_mfma_f32_32x32x16_f16 a[16:31], v[44:47], v[112:115], a[16:31]
	s_add_u32 m0, s48, 0x103c0
	s_add_u32 s44, s44, 0x1800
	s_addc_u32 s45, s45, 0
	global_load_lds_dwordx4 v78, s[44:45]
	ds_read_b128 v[44:47], v84 offset:10240
	v_mfma_f32_32x32x16_f16 a[0:15], v[48:51], v[112:115], a[0:15]
	ds_read_b128 v[48:51], v84 offset:11264
	s_waitcnt lgkmcnt(6)
	v_mfma_f32_32x32x16_f16 a[80:95], v[4:7], v[52:55], a[80:95]
	v_mfma_f32_32x32x16_f16 a[64:79], v[8:11], v[52:55], a[64:79]
	v_mfma_f32_32x32x16_f16 a[48:63], v[12:15], v[52:55], a[48:63]
	s_waitcnt vmcnt(10)
	s_waitcnt lgkmcnt(0)
	s_barrier
	ds_read_b128 v[4:7], v84 offset:12288
	ds_read_b128 v[8:11], v84 offset:13312
	ds_read_b128 v[12:15], v84 offset:14336
	v_mfma_f32_32x32x16_f16 a[32:47], v[16:19], v[52:55], a[32:47]
	ds_read_b128 v[16:19], v84 offset:15360
	v_mfma_f32_32x32x16_f16 a[16:31], v[20:23], v[52:55], a[16:31]
	ds_read_b128 v[20:23], v84 offset:16384
	v_mfma_f32_32x32x16_f16 a[0:15], v[24:27], v[52:55], a[0:15]
	ds_read_b128 v[24:27], v84 offset:17408
	v_mfma_f32_32x32x16_f16 a[80:95], v[28:31], v[56:59], a[80:95]
	s_add_u32 m0, s46, 0x0
	s_add_u32 s40, s40, 0x1800
	s_addc_u32 s41, s41, 0
	global_load_lds_dwordx4 v76, s[40:41]
	ds_read_b128 v[28:31], v84 offset:18432
	v_mfma_f32_32x32x16_f16 a[64:79], v[32:35], v[56:59], a[64:79]
	ds_read_b128 v[32:35], v84 offset:19456
	v_mfma_f32_32x32x16_f16 a[48:63], v[36:39], v[56:59], a[48:63]
	s_add_u32 m0, s47, 0x0
	s_add_u32 s42, s42, 0x1800
	s_addc_u32 s43, s43, 0
	global_load_lds_dwordx4 v77, s[42:43]
	ds_read_b128 v[36:39], v84 offset:20480
	v_mfma_f32_32x32x16_f16 a[32:47], v[40:43], v[56:59], a[32:47]
	ds_read_b128 v[40:43], v84 offset:21504
	v_mfma_f32_32x32x16_f16 a[16:31], v[44:47], v[56:59], a[16:31]
	s_add_u32 m0, s48, 0x0
	s_add_u32 s44, s44, 0x1800
	s_addc_u32 s45, s45, 0
	global_load_lds_dwordx4 v78, s[44:45]
	ds_read_b128 v[44:47], v84 offset:22528
	v_mfma_f32_32x32x16_f16 a[0:15], v[48:51], v[56:59], a[0:15]
	ds_read_b128 v[48:51], v84 offset:23552
	s_waitcnt lgkmcnt(6)
	v_mfma_f32_32x32x16_f16 a[80:95], v[4:7], v[60:63], a[80:95]
	s_waitcnt vmcnt(23)
	ds_write_b128 v81, v[116:119]
	ds_write_b128 v81, v[120:123] offset:1024
	v_mfma_f32_32x32x16_f16 a[64:79], v[8:11], v[60:63], a[64:79]
	ds_write_b128 v81, v[124:127] offset:2048
	ds_write_b128 v81, v[128:131] offset:3072
	v_mfma_f32_32x32x16_f16 a[48:63], v[12:15], v[60:63], a[48:63]
	ds_read_b128 v[100:103], v95
	ds_read_b128 v[104:107], v96
	ds_read_b128 v[108:111], v97
	ds_read_b128 v[112:115], v94
	s_waitcnt vmcnt(10)
	s_waitcnt lgkmcnt(8)
	s_barrier
	ds_read_b128 v[4:7], v84 offset:54208
	ds_read_b128 v[8:11], v84 offset:55232
	ds_read_b128 v[12:15], v84 offset:56256
	v_mfma_f32_32x32x16_f16 a[32:47], v[16:19], v[60:63], a[32:47]
	ds_read_b128 v[16:19], v84 offset:57280
	v_mfma_f32_32x32x16_f16 a[16:31], v[20:23], v[60:63], a[16:31]
	ds_read_b128 v[20:23], v84 offset:58304
	v_mfma_f32_32x32x16_f16 a[0:15], v[24:27], v[60:63], a[0:15]
	ds_read_b128 v[24:27], v84 offset:59328
	s_waitcnt lgkmcnt(6)
	v_mfma_f32_32x32x16_f16 a[80:95], v[28:31], v[0:3], a[80:95]
	s_add_u32 m0, s46, 0x3000
	s_add_u32 s40, s40, 0x1800
	s_addc_u32 s41, s41, 0
	global_load_lds_dwordx4 v76, s[40:41]
	ds_read_b128 v[28:31], v84 offset:60352
	v_mfma_f32_32x32x16_f16 a[64:79], v[32:35], v[0:3], a[64:79]
	global_load_dwordx4 v[116:119], v64, s[4:5] offset:768
	global_load_dwordx4 v[120:123], v66, s[4:5] offset:768
	ds_read_b128 v[32:35], v84 offset:61376
	v_mfma_f32_32x32x16_f16 a[48:63], v[36:39], v[0:3], a[48:63]
	s_add_u32 m0, s47, 0x3000
	s_add_u32 s42, s42, 0x1800
	s_addc_u32 s43, s43, 0
	global_load_lds_dwordx4 v77, s[42:43]
	ds_read_b128 v[36:39], v84 offset:62400
	v_mfma_f32_32x32x16_f16 a[32:47], v[40:43], v[0:3], a[32:47]
	global_load_dwordx4 v[124:127], v68, s[4:5] offset:768
	global_load_dwordx4 v[128:131], v70, s[4:5] offset:768
	ds_read_b128 v[40:43], v84 offset:63424
	v_mfma_f32_32x32x16_f16 a[16:31], v[44:47], v[0:3], a[16:31]
	s_add_u32 m0, s48, 0x3000
	s_add_u32 s44, s44, 0x1800
	s_addc_u32 s45, s45, 0
	global_load_lds_dwordx4 v78, s[44:45]
	ds_read_b128 v[44:47], v84 offset:64448
	v_mfma_f32_32x32x16_f16 a[0:15], v[48:51], v[0:3], a[0:15]
	ds_read_b128 v[48:51], v84 offset:65472
	s_waitcnt lgkmcnt(6)
	v_mfma_f32_32x32x16_f16 a[80:95], v[4:7], v[100:103], a[80:95]
	v_mfma_f32_32x32x16_f16 a[64:79], v[8:11], v[100:103], a[64:79]
	v_mfma_f32_32x32x16_f16 a[48:63], v[12:15], v[100:103], a[48:63]
	s_waitcnt vmcnt(10)
	s_waitcnt lgkmcnt(0)
	s_barrier
	ds_read_b128 v[4:7], v98
	ds_read_b128 v[8:11], v98 offset:1024
	ds_read_b128 v[12:15], v98 offset:2048
	v_mfma_f32_32x32x16_f16 a[32:47], v[16:19], v[100:103], a[32:47]
	ds_read_b128 v[16:19], v98 offset:3072
	v_mfma_f32_32x32x16_f16 a[16:31], v[20:23], v[100:103], a[16:31]
	ds_read_b128 v[20:23], v98 offset:4096
	v_mfma_f32_32x32x16_f16 a[0:15], v[24:27], v[100:103], a[0:15]
	ds_read_b128 v[24:27], v98 offset:5120
	v_mfma_f32_32x32x16_f16 a[80:95], v[28:31], v[104:107], a[80:95]
	s_add_u32 m0, s46, 0xd3c0
	s_add_u32 s40, s40, 0x1800
	s_addc_u32 s41, s41, 0
	global_load_lds_dwordx4 v76, s[40:41]
	ds_read_b128 v[28:31], v98 offset:6144
	v_mfma_f32_32x32x16_f16 a[64:79], v[32:35], v[104:107], a[64:79]
	ds_read_b128 v[32:35], v98 offset:7168
	v_mfma_f32_32x32x16_f16 a[48:63], v[36:39], v[104:107], a[48:63]
	s_add_u32 m0, s47, 0xd3c0
	s_add_u32 s42, s42, 0x1800
	s_addc_u32 s43, s43, 0
	global_load_lds_dwordx4 v77, s[42:43]
	ds_read_b128 v[36:39], v98 offset:8192
	v_mfma_f32_32x32x16_f16 a[32:47], v[40:43], v[104:107], a[32:47]
	ds_read_b128 v[40:43], v98 offset:9216
	v_mfma_f32_32x32x16_f16 a[16:31], v[44:47], v[104:107], a[16:31]
	s_add_u32 m0, s48, 0xd3c0
	s_add_u32 s44, s44, 0x1800
	s_addc_u32 s45, s45, 0
	global_load_lds_dwordx4 v78, s[44:45]
	ds_read_b128 v[44:47], v98 offset:10240
	v_mfma_f32_32x32x16_f16 a[0:15], v[48:51], v[104:107], a[0:15]
	ds_read_b128 v[48:51], v98 offset:11264
	s_waitcnt lgkmcnt(6)
	v_mfma_f32_32x32x16_f16 a[80:95], v[4:7], v[108:111], a[80:95]
	s_waitcnt vmcnt(24)
	ds_write_b128 v81, v[132:135]
	ds_write_b128 v81, v[136:139] offset:1024
	v_mfma_f32_32x32x16_f16 a[64:79], v[8:11], v[108:111], a[64:79]
	ds_write_b128 v81, v[140:143] offset:2048
	ds_write_b128 v81, v[144:147] offset:3072
	v_mfma_f32_32x32x16_f16 a[48:63], v[12:15], v[108:111], a[48:63]
	ds_read_b128 v[52:55], v95
	ds_read_b128 v[56:59], v96
	ds_read_b128 v[60:63], v97
	ds_read_b128 v[0:3], v94
	s_waitcnt vmcnt(10)
	s_waitcnt lgkmcnt(8)
	s_barrier
	ds_read_b128 v[4:7], v84 offset:0
	ds_read_b128 v[8:11], v84 offset:1024
	ds_read_b128 v[12:15], v84 offset:2048
	v_mfma_f32_32x32x16_f16 a[32:47], v[16:19], v[108:111], a[32:47]
	ds_read_b128 v[16:19], v84 offset:3072
	v_mfma_f32_32x32x16_f16 a[16:31], v[20:23], v[108:111], a[16:31]
	ds_read_b128 v[20:23], v84 offset:4096
	v_mfma_f32_32x32x16_f16 a[0:15], v[24:27], v[108:111], a[0:15]
	ds_read_b128 v[24:27], v84 offset:5120
	s_waitcnt lgkmcnt(6)
	v_mfma_f32_32x32x16_f16 a[80:95], v[28:31], v[112:115], a[80:95]
	s_add_u32 m0, s46, 0x103c0
	s_add_u32 s40, s40, 0x1800
	s_addc_u32 s41, s41, 0
	global_load_lds_dwordx4 v76, s[40:41]
	ds_read_b128 v[28:31], v84 offset:6144
	v_mfma_f32_32x32x16_f16 a[64:79], v[32:35], v[112:115], a[64:79]
	global_load_dwordx4 v[132:135], v64, s[4:5] offset:896
	global_load_dwordx4 v[136:139], v66, s[4:5] offset:896
	ds_read_b128 v[32:35], v84 offset:7168
	v_mfma_f32_32x32x16_f16 a[48:63], v[36:39], v[112:115], a[48:63]
	s_add_u32 m0, s47, 0x103c0
	s_add_u32 s42, s42, 0x1800
	s_addc_u32 s43, s43, 0
	global_load_lds_dwordx4 v77, s[42:43]
	ds_read_b128 v[36:39], v84 offset:8192
	v_mfma_f32_32x32x16_f16 a[32:47], v[40:43], v[112:115], a[32:47]
	global_load_dwordx4 v[140:143], v68, s[4:5] offset:896
	global_load_dwordx4 v[144:147], v70, s[4:5] offset:896
	ds_read_b128 v[40:43], v84 offset:9216
	v_mfma_f32_32x32x16_f16 a[16:31], v[44:47], v[112:115], a[16:31]
	s_add_u32 m0, s48, 0x103c0
	s_add_u32 s44, s44, 0x1800
	s_addc_u32 s45, s45, 0
	global_load_lds_dwordx4 v78, s[44:45]
	ds_read_b128 v[44:47], v84 offset:10240
	v_mfma_f32_32x32x16_f16 a[0:15], v[48:51], v[112:115], a[0:15]
	ds_read_b128 v[48:51], v84 offset:11264
	s_waitcnt lgkmcnt(6)
	v_mfma_f32_32x32x16_f16 a[80:95], v[4:7], v[52:55], a[80:95]
	v_mfma_f32_32x32x16_f16 a[64:79], v[8:11], v[52:55], a[64:79]
	v_mfma_f32_32x32x16_f16 a[48:63], v[12:15], v[52:55], a[48:63]
	s_waitcnt vmcnt(10)
	s_waitcnt lgkmcnt(0)
	s_barrier
	ds_read_b128 v[4:7], v84 offset:12288
	ds_read_b128 v[8:11], v84 offset:13312
	ds_read_b128 v[12:15], v84 offset:14336
	v_mfma_f32_32x32x16_f16 a[32:47], v[16:19], v[52:55], a[32:47]
	ds_read_b128 v[16:19], v84 offset:15360
	v_mfma_f32_32x32x16_f16 a[16:31], v[20:23], v[52:55], a[16:31]
	ds_read_b128 v[20:23], v84 offset:16384
	v_mfma_f32_32x32x16_f16 a[0:15], v[24:27], v[52:55], a[0:15]
	ds_read_b128 v[24:27], v84 offset:17408
	v_mfma_f32_32x32x16_f16 a[80:95], v[28:31], v[56:59], a[80:95]
	s_add_u32 m0, s46, 0x0
	s_add_u32 s40, s40, 0x1800
	s_addc_u32 s41, s41, 0
	global_load_lds_dwordx4 v76, s[40:41]
	ds_read_b128 v[28:31], v84 offset:18432
	v_mfma_f32_32x32x16_f16 a[64:79], v[32:35], v[56:59], a[64:79]
	ds_read_b128 v[32:35], v84 offset:19456
	v_mfma_f32_32x32x16_f16 a[48:63], v[36:39], v[56:59], a[48:63]
	s_add_u32 m0, s47, 0x0
	s_add_u32 s42, s42, 0x1800
	s_addc_u32 s43, s43, 0
	global_load_lds_dwordx4 v77, s[42:43]
	ds_read_b128 v[36:39], v84 offset:20480
	v_mfma_f32_32x32x16_f16 a[32:47], v[40:43], v[56:59], a[32:47]
	ds_read_b128 v[40:43], v84 offset:21504
	v_mfma_f32_32x32x16_f16 a[16:31], v[44:47], v[56:59], a[16:31]
	s_add_u32 m0, s48, 0x0
	s_add_u32 s44, s44, 0x1800
	s_addc_u32 s45, s45, 0
	global_load_lds_dwordx4 v78, s[44:45]
	ds_read_b128 v[44:47], v84 offset:22528
	v_mfma_f32_32x32x16_f16 a[0:15], v[48:51], v[56:59], a[0:15]
	ds_read_b128 v[48:51], v84 offset:23552
	s_waitcnt lgkmcnt(6)
	v_mfma_f32_32x32x16_f16 a[80:95], v[4:7], v[60:63], a[80:95]
	s_waitcnt vmcnt(24)
	ds_write_b128 v81, v[148:151]
	ds_write_b128 v81, v[152:155] offset:1024
	v_mfma_f32_32x32x16_f16 a[64:79], v[8:11], v[60:63], a[64:79]
	ds_write_b128 v81, v[156:159] offset:2048
	ds_write_b128 v81, v[72:75] offset:3072
	v_mfma_f32_32x32x16_f16 a[48:63], v[12:15], v[60:63], a[48:63]
	ds_read_b128 v[100:103], v95
	ds_read_b128 v[104:107], v96
	ds_read_b128 v[108:111], v97
	ds_read_b128 v[112:115], v94
	s_waitcnt vmcnt(10)
	s_waitcnt lgkmcnt(8)
	s_barrier
	ds_read_b128 v[4:7], v84 offset:54208
	ds_read_b128 v[8:11], v84 offset:55232
	ds_read_b128 v[12:15], v84 offset:56256
	v_mfma_f32_32x32x16_f16 a[32:47], v[16:19], v[60:63], a[32:47]
	ds_read_b128 v[16:19], v84 offset:57280
	v_mfma_f32_32x32x16_f16 a[16:31], v[20:23], v[60:63], a[16:31]
	ds_read_b128 v[20:23], v84 offset:58304
	v_mfma_f32_32x32x16_f16 a[0:15], v[24:27], v[60:63], a[0:15]
	ds_read_b128 v[24:27], v84 offset:59328
	s_waitcnt lgkmcnt(6)
	v_mfma_f32_32x32x16_f16 a[80:95], v[28:31], v[0:3], a[80:95]
	s_add_u32 m0, s46, 0x3000
	s_add_u32 s40, s40, 0x1800
	s_addc_u32 s41, s41, 0
	global_load_lds_dwordx4 v76, s[40:41]
	ds_read_b128 v[28:31], v84 offset:60352
	v_mfma_f32_32x32x16_f16 a[64:79], v[32:35], v[0:3], a[64:79]
	global_load_dwordx4 v[148:151], v64, s[4:5] offset:1024
	global_load_dwordx4 v[152:155], v66, s[4:5] offset:1024
	ds_read_b128 v[32:35], v84 offset:61376
	v_mfma_f32_32x32x16_f16 a[48:63], v[36:39], v[0:3], a[48:63]
	s_add_u32 m0, s47, 0x3000
	s_add_u32 s42, s42, 0x1800
	s_addc_u32 s43, s43, 0
	global_load_lds_dwordx4 v77, s[42:43]
	ds_read_b128 v[36:39], v84 offset:62400
	v_mfma_f32_32x32x16_f16 a[32:47], v[40:43], v[0:3], a[32:47]
	global_load_dwordx4 v[156:159], v68, s[4:5] offset:1024
	global_load_dwordx4 v[72:75], v70, s[4:5] offset:1024
	ds_read_b128 v[40:43], v84 offset:63424
	v_mfma_f32_32x32x16_f16 a[16:31], v[44:47], v[0:3], a[16:31]
	s_add_u32 m0, s48, 0x3000
	s_add_u32 s44, s44, 0x1800
	s_addc_u32 s45, s45, 0
	global_load_lds_dwordx4 v78, s[44:45]
	ds_read_b128 v[44:47], v84 offset:64448
	v_mfma_f32_32x32x16_f16 a[0:15], v[48:51], v[0:3], a[0:15]
	ds_read_b128 v[48:51], v84 offset:65472
	s_waitcnt lgkmcnt(6)
	v_mfma_f32_32x32x16_f16 a[80:95], v[4:7], v[100:103], a[80:95]
	v_mfma_f32_32x32x16_f16 a[64:79], v[8:11], v[100:103], a[64:79]
	v_mfma_f32_32x32x16_f16 a[48:63], v[12:15], v[100:103], a[48:63]
	s_waitcnt vmcnt(10)
	s_waitcnt lgkmcnt(0)
	s_barrier
	ds_read_b128 v[4:7], v98
	ds_read_b128 v[8:11], v98 offset:1024
	ds_read_b128 v[12:15], v98 offset:2048
	v_mfma_f32_32x32x16_f16 a[32:47], v[16:19], v[100:103], a[32:47]
	ds_read_b128 v[16:19], v98 offset:3072
	v_mfma_f32_32x32x16_f16 a[16:31], v[20:23], v[100:103], a[16:31]
	ds_read_b128 v[20:23], v98 offset:4096
	v_mfma_f32_32x32x16_f16 a[0:15], v[24:27], v[100:103], a[0:15]
	ds_read_b128 v[24:27], v98 offset:5120
	v_mfma_f32_32x32x16_f16 a[80:95], v[28:31], v[104:107], a[80:95]
	s_add_u32 m0, s46, 0xd3c0
	s_add_u32 s40, s40, 0x1800
	s_addc_u32 s41, s41, 0
	global_load_lds_dwordx4 v76, s[40:41]
	ds_read_b128 v[28:31], v98 offset:6144
	v_mfma_f32_32x32x16_f16 a[64:79], v[32:35], v[104:107], a[64:79]
	ds_read_b128 v[32:35], v98 offset:7168
	v_mfma_f32_32x32x16_f16 a[48:63], v[36:39], v[104:107], a[48:63]
	s_add_u32 m0, s47, 0xd3c0
	s_add_u32 s42, s42, 0x1800
	s_addc_u32 s43, s43, 0
	global_load_lds_dwordx4 v77, s[42:43]
	ds_read_b128 v[36:39], v98 offset:8192
	v_mfma_f32_32x32x16_f16 a[32:47], v[40:43], v[104:107], a[32:47]
	ds_read_b128 v[40:43], v98 offset:9216
	v_mfma_f32_32x32x16_f16 a[16:31], v[44:47], v[104:107], a[16:31]
	s_add_u32 m0, s48, 0xd3c0
	s_add_u32 s44, s44, 0x1800
	s_addc_u32 s45, s45, 0
	global_load_lds_dwordx4 v78, s[44:45]
	ds_read_b128 v[44:47], v98 offset:10240
	v_mfma_f32_32x32x16_f16 a[0:15], v[48:51], v[104:107], a[0:15]
	ds_read_b128 v[48:51], v98 offset:11264
	s_waitcnt lgkmcnt(6)
	v_mfma_f32_32x32x16_f16 a[80:95], v[4:7], v[108:111], a[80:95]
	s_waitcnt vmcnt(24)
	ds_write_b128 v81, v[116:119]
	ds_write_b128 v81, v[120:123] offset:1024
	v_mfma_f32_32x32x16_f16 a[64:79], v[8:11], v[108:111], a[64:79]
	ds_write_b128 v81, v[124:127] offset:2048
	ds_write_b128 v81, v[128:131] offset:3072
	v_mfma_f32_32x32x16_f16 a[48:63], v[12:15], v[108:111], a[48:63]
	ds_read_b128 v[52:55], v95
	ds_read_b128 v[56:59], v96
	ds_read_b128 v[60:63], v97
	ds_read_b128 v[0:3], v94
	s_waitcnt vmcnt(10)
	s_waitcnt lgkmcnt(8)
	s_barrier
	ds_read_b128 v[4:7], v84 offset:0
	ds_read_b128 v[8:11], v84 offset:1024
	ds_read_b128 v[12:15], v84 offset:2048
	v_mfma_f32_32x32x16_f16 a[32:47], v[16:19], v[108:111], a[32:47]
	ds_read_b128 v[16:19], v84 offset:3072
	v_mfma_f32_32x32x16_f16 a[16:31], v[20:23], v[108:111], a[16:31]
	ds_read_b128 v[20:23], v84 offset:4096
	v_mfma_f32_32x32x16_f16 a[0:15], v[24:27], v[108:111], a[0:15]
	ds_read_b128 v[24:27], v84 offset:5120
	s_waitcnt lgkmcnt(6)
	v_mfma_f32_32x32x16_f16 a[80:95], v[28:31], v[112:115], a[80:95]
	s_add_u32 m0, s46, 0x103c0
	s_add_u32 s40, s40, 0x1800
	s_addc_u32 s41, s41, 0
	global_load_lds_dwordx4 v76, s[40:41]
	ds_read_b128 v[28:31], v84 offset:6144
	v_mfma_f32_32x32x16_f16 a[64:79], v[32:35], v[112:115], a[64:79]
	global_load_dwordx4 v[116:119], v64, s[4:5] offset:1152
	global_load_dwordx4 v[120:123], v66, s[4:5] offset:1152
	ds_read_b128 v[32:35], v84 offset:7168
	v_mfma_f32_32x32x16_f16 a[48:63], v[36:39], v[112:115], a[48:63]
	s_add_u32 m0, s47, 0x103c0
	s_add_u32 s42, s42, 0x1800
	s_addc_u32 s43, s43, 0
	global_load_lds_dwordx4 v77, s[42:43]
	ds_read_b128 v[36:39], v84 offset:8192
	v_mfma_f32_32x32x16_f16 a[32:47], v[40:43], v[112:115], a[32:47]
	global_load_dwordx4 v[124:127], v68, s[4:5] offset:1152
	global_load_dwordx4 v[128:131], v70, s[4:5] offset:1152
	ds_read_b128 v[40:43], v84 offset:9216
	v_mfma_f32_32x32x16_f16 a[16:31], v[44:47], v[112:115], a[16:31]
	s_add_u32 m0, s48, 0x103c0
	s_add_u32 s44, s44, 0x1800
	s_addc_u32 s45, s45, 0
	global_load_lds_dwordx4 v78, s[44:45]
	ds_read_b128 v[44:47], v84 offset:10240
	v_mfma_f32_32x32x16_f16 a[0:15], v[48:51], v[112:115], a[0:15]
	ds_read_b128 v[48:51], v84 offset:11264
	s_waitcnt lgkmcnt(6)
	v_mfma_f32_32x32x16_f16 a[80:95], v[4:7], v[52:55], a[80:95]
	v_mfma_f32_32x32x16_f16 a[64:79], v[8:11], v[52:55], a[64:79]
	v_mfma_f32_32x32x16_f16 a[48:63], v[12:15], v[52:55], a[48:63]
	s_waitcnt vmcnt(10)
	s_waitcnt lgkmcnt(0)
	s_barrier
	ds_read_b128 v[4:7], v84 offset:12288
	ds_read_b128 v[8:11], v84 offset:13312
	ds_read_b128 v[12:15], v84 offset:14336
	v_mfma_f32_32x32x16_f16 a[32:47], v[16:19], v[52:55], a[32:47]
	ds_read_b128 v[16:19], v84 offset:15360
	v_mfma_f32_32x32x16_f16 a[16:31], v[20:23], v[52:55], a[16:31]
	ds_read_b128 v[20:23], v84 offset:16384
	v_mfma_f32_32x32x16_f16 a[0:15], v[24:27], v[52:55], a[0:15]
	ds_read_b128 v[24:27], v84 offset:17408
	v_mfma_f32_32x32x16_f16 a[80:95], v[28:31], v[56:59], a[80:95]
	s_add_u32 m0, s46, 0x0
	s_add_u32 s40, s40, 0x1800
	s_addc_u32 s41, s41, 0
	global_load_lds_dwordx4 v76, s[40:41]
	ds_read_b128 v[28:31], v84 offset:18432
	v_mfma_f32_32x32x16_f16 a[64:79], v[32:35], v[56:59], a[64:79]
	ds_read_b128 v[32:35], v84 offset:19456
	v_mfma_f32_32x32x16_f16 a[48:63], v[36:39], v[56:59], a[48:63]
	s_add_u32 m0, s47, 0x0
	s_add_u32 s42, s42, 0x1800
	s_addc_u32 s43, s43, 0
	global_load_lds_dwordx4 v77, s[42:43]
	ds_read_b128 v[36:39], v84 offset:20480
	v_mfma_f32_32x32x16_f16 a[32:47], v[40:43], v[56:59], a[32:47]
	ds_read_b128 v[40:43], v84 offset:21504
	v_mfma_f32_32x32x16_f16 a[16:31], v[44:47], v[56:59], a[16:31]
	s_add_u32 m0, s48, 0x0
	s_add_u32 s44, s44, 0x1800
	s_addc_u32 s45, s45, 0
	global_load_lds_dwordx4 v78, s[44:45]
	ds_read_b128 v[44:47], v84 offset:22528
	v_mfma_f32_32x32x16_f16 a[0:15], v[48:51], v[56:59], a[0:15]
	ds_read_b128 v[48:51], v84 offset:23552
	s_waitcnt lgkmcnt(6)
	v_mfma_f32_32x32x16_f16 a[80:95], v[4:7], v[60:63], a[80:95]
	s_waitcnt vmcnt(24)
	ds_write_b128 v81, v[132:135]
	ds_write_b128 v81, v[136:139] offset:1024
	v_mfma_f32_32x32x16_f16 a[64:79], v[8:11], v[60:63], a[64:79]
	ds_write_b128 v81, v[140:143] offset:2048
	ds_write_b128 v81, v[144:147] offset:3072
	v_mfma_f32_32x32x16_f16 a[48:63], v[12:15], v[60:63], a[48:63]
	ds_read_b128 v[100:103], v95
	ds_read_b128 v[104:107], v96
	ds_read_b128 v[108:111], v97
	ds_read_b128 v[112:115], v94
	s_waitcnt vmcnt(10)
	s_waitcnt lgkmcnt(8)
	s_barrier
	ds_read_b128 v[4:7], v84 offset:54208
	ds_read_b128 v[8:11], v84 offset:55232
	ds_read_b128 v[12:15], v84 offset:56256
	v_mfma_f32_32x32x16_f16 a[32:47], v[16:19], v[60:63], a[32:47]
	ds_read_b128 v[16:19], v84 offset:57280
	v_mfma_f32_32x32x16_f16 a[16:31], v[20:23], v[60:63], a[16:31]
	ds_read_b128 v[20:23], v84 offset:58304
	v_mfma_f32_32x32x16_f16 a[0:15], v[24:27], v[60:63], a[0:15]
	ds_read_b128 v[24:27], v84 offset:59328
	s_waitcnt lgkmcnt(6)
	v_mfma_f32_32x32x16_f16 a[80:95], v[28:31], v[0:3], a[80:95]
	s_add_u32 m0, s46, 0x3000
	s_add_u32 s40, s40, 0x1800
	s_addc_u32 s41, s41, 0
	global_load_lds_dwordx4 v76, s[40:41]
	ds_read_b128 v[28:31], v84 offset:60352
	v_mfma_f32_32x32x16_f16 a[64:79], v[32:35], v[0:3], a[64:79]
	global_load_dwordx4 v[132:135], v64, s[4:5] offset:1280
	global_load_dwordx4 v[136:139], v66, s[4:5] offset:1280
	ds_read_b128 v[32:35], v84 offset:61376
	v_mfma_f32_32x32x16_f16 a[48:63], v[36:39], v[0:3], a[48:63]
	s_add_u32 m0, s47, 0x3000
	s_add_u32 s42, s42, 0x1800
	s_addc_u32 s43, s43, 0
	global_load_lds_dwordx4 v77, s[42:43]
	ds_read_b128 v[36:39], v84 offset:62400
	v_mfma_f32_32x32x16_f16 a[32:47], v[40:43], v[0:3], a[32:47]
	global_load_dwordx4 v[140:143], v68, s[4:5] offset:1280
	global_load_dwordx4 v[144:147], v70, s[4:5] offset:1280
	ds_read_b128 v[40:43], v84 offset:63424
	v_mfma_f32_32x32x16_f16 a[16:31], v[44:47], v[0:3], a[16:31]
	s_add_u32 m0, s48, 0x3000
	s_add_u32 s44, s44, 0x1800
	s_addc_u32 s45, s45, 0
	global_load_lds_dwordx4 v78, s[44:45]
	ds_read_b128 v[44:47], v84 offset:64448
	v_mfma_f32_32x32x16_f16 a[0:15], v[48:51], v[0:3], a[0:15]
	ds_read_b128 v[48:51], v84 offset:65472
	s_waitcnt lgkmcnt(6)
	v_mfma_f32_32x32x16_f16 a[80:95], v[4:7], v[100:103], a[80:95]
	v_mfma_f32_32x32x16_f16 a[64:79], v[8:11], v[100:103], a[64:79]
	v_mfma_f32_32x32x16_f16 a[48:63], v[12:15], v[100:103], a[48:63]
	s_waitcnt vmcnt(10)
	s_waitcnt lgkmcnt(0)
	s_barrier
	ds_read_b128 v[4:7], v98
	ds_read_b128 v[8:11], v98 offset:1024
	ds_read_b128 v[12:15], v98 offset:2048
	v_mfma_f32_32x32x16_f16 a[32:47], v[16:19], v[100:103], a[32:47]
	ds_read_b128 v[16:19], v98 offset:3072
	v_mfma_f32_32x32x16_f16 a[16:31], v[20:23], v[100:103], a[16:31]
	ds_read_b128 v[20:23], v98 offset:4096
	v_mfma_f32_32x32x16_f16 a[0:15], v[24:27], v[100:103], a[0:15]
	ds_read_b128 v[24:27], v98 offset:5120
	v_mfma_f32_32x32x16_f16 a[80:95], v[28:31], v[104:107], a[80:95]
	s_add_u32 m0, s46, 0xd3c0
	s_add_u32 s40, s40, 0x1800
	s_addc_u32 s41, s41, 0
	global_load_lds_dwordx4 v76, s[40:41]
	ds_read_b128 v[28:31], v98 offset:6144
	v_mfma_f32_32x32x16_f16 a[64:79], v[32:35], v[104:107], a[64:79]
	ds_read_b128 v[32:35], v98 offset:7168
	v_mfma_f32_32x32x16_f16 a[48:63], v[36:39], v[104:107], a[48:63]
	s_add_u32 m0, s47, 0xd3c0
	s_add_u32 s42, s42, 0x1800
	s_addc_u32 s43, s43, 0
	global_load_lds_dwordx4 v77, s[42:43]
	ds_read_b128 v[36:39], v98 offset:8192
	v_mfma_f32_32x32x16_f16 a[32:47], v[40:43], v[104:107], a[32:47]
	ds_read_b128 v[40:43], v98 offset:9216
	v_mfma_f32_32x32x16_f16 a[16:31], v[44:47], v[104:107], a[16:31]
	s_add_u32 m0, s48, 0xd3c0
	s_add_u32 s44, s44, 0x1800
	s_addc_u32 s45, s45, 0
	global_load_lds_dwordx4 v78, s[44:45]
	ds_read_b128 v[44:47], v98 offset:10240
	v_mfma_f32_32x32x16_f16 a[0:15], v[48:51], v[104:107], a[0:15]
	ds_read_b128 v[48:51], v98 offset:11264
	s_waitcnt lgkmcnt(6)
	v_mfma_f32_32x32x16_f16 a[80:95], v[4:7], v[108:111], a[80:95]
	s_waitcnt vmcnt(24)
	ds_write_b128 v81, v[148:151]
	ds_write_b128 v81, v[152:155] offset:1024
	v_mfma_f32_32x32x16_f16 a[64:79], v[8:11], v[108:111], a[64:79]
	ds_write_b128 v81, v[156:159] offset:2048
	ds_write_b128 v81, v[72:75] offset:3072
	v_mfma_f32_32x32x16_f16 a[48:63], v[12:15], v[108:111], a[48:63]
	ds_read_b128 v[52:55], v95
	ds_read_b128 v[56:59], v96
	ds_read_b128 v[60:63], v97
	ds_read_b128 v[0:3], v94
	s_waitcnt vmcnt(10)
	s_waitcnt lgkmcnt(8)
	s_barrier
	ds_read_b128 v[4:7], v84 offset:0
	ds_read_b128 v[8:11], v84 offset:1024
	ds_read_b128 v[12:15], v84 offset:2048
	v_mfma_f32_32x32x16_f16 a[32:47], v[16:19], v[108:111], a[32:47]
	ds_read_b128 v[16:19], v84 offset:3072
	v_mfma_f32_32x32x16_f16 a[16:31], v[20:23], v[108:111], a[16:31]
	ds_read_b128 v[20:23], v84 offset:4096
	v_mfma_f32_32x32x16_f16 a[0:15], v[24:27], v[108:111], a[0:15]
	ds_read_b128 v[24:27], v84 offset:5120
	s_waitcnt lgkmcnt(6)
	v_mfma_f32_32x32x16_f16 a[80:95], v[28:31], v[112:115], a[80:95]
	s_add_u32 m0, s46, 0x103c0
	s_add_u32 s40, s40, 0x1800
	s_addc_u32 s41, s41, 0
	global_load_lds_dwordx4 v76, s[40:41]
	ds_read_b128 v[28:31], v84 offset:6144
	v_mfma_f32_32x32x16_f16 a[64:79], v[32:35], v[112:115], a[64:79]
	global_load_dwordx4 v[148:151], v64, s[4:5] offset:1408
	global_load_dwordx4 v[152:155], v66, s[4:5] offset:1408
	ds_read_b128 v[32:35], v84 offset:7168
	v_mfma_f32_32x32x16_f16 a[48:63], v[36:39], v[112:115], a[48:63]
	s_add_u32 m0, s47, 0x103c0
	s_add_u32 s42, s42, 0x1800
	s_addc_u32 s43, s43, 0
	global_load_lds_dwordx4 v77, s[42:43]
	ds_read_b128 v[36:39], v84 offset:8192
	v_mfma_f32_32x32x16_f16 a[32:47], v[40:43], v[112:115], a[32:47]
	global_load_dwordx4 v[156:159], v68, s[4:5] offset:1408
	global_load_dwordx4 v[72:75], v70, s[4:5] offset:1408
	ds_read_b128 v[40:43], v84 offset:9216
	v_mfma_f32_32x32x16_f16 a[16:31], v[44:47], v[112:115], a[16:31]
	s_add_u32 m0, s48, 0x103c0
	s_add_u32 s44, s44, 0x1800
	s_addc_u32 s45, s45, 0
	global_load_lds_dwordx4 v78, s[44:45]
	ds_read_b128 v[44:47], v84 offset:10240
	v_mfma_f32_32x32x16_f16 a[0:15], v[48:51], v[112:115], a[0:15]
	ds_read_b128 v[48:51], v84 offset:11264
	s_waitcnt lgkmcnt(6)
	v_mfma_f32_32x32x16_f16 a[80:95], v[4:7], v[52:55], a[80:95]
	v_mfma_f32_32x32x16_f16 a[64:79], v[8:11], v[52:55], a[64:79]
	v_mfma_f32_32x32x16_f16 a[48:63], v[12:15], v[52:55], a[48:63]
	s_waitcnt vmcnt(10)
	s_waitcnt lgkmcnt(0)
	s_barrier
	ds_read_b128 v[4:7], v84 offset:12288
	ds_read_b128 v[8:11], v84 offset:13312
	ds_read_b128 v[12:15], v84 offset:14336
	v_mfma_f32_32x32x16_f16 a[32:47], v[16:19], v[52:55], a[32:47]
	ds_read_b128 v[16:19], v84 offset:15360
	v_mfma_f32_32x32x16_f16 a[16:31], v[20:23], v[52:55], a[16:31]
	ds_read_b128 v[20:23], v84 offset:16384
	v_mfma_f32_32x32x16_f16 a[0:15], v[24:27], v[52:55], a[0:15]
	ds_read_b128 v[24:27], v84 offset:17408
	v_mfma_f32_32x32x16_f16 a[80:95], v[28:31], v[56:59], a[80:95]
	s_add_u32 m0, s46, 0x0
	s_add_u32 s40, s40, 0x1800
	s_addc_u32 s41, s41, 0
	global_load_lds_dwordx4 v76, s[40:41]
	ds_read_b128 v[28:31], v84 offset:18432
	v_mfma_f32_32x32x16_f16 a[64:79], v[32:35], v[56:59], a[64:79]
	ds_read_b128 v[32:35], v84 offset:19456
	v_mfma_f32_32x32x16_f16 a[48:63], v[36:39], v[56:59], a[48:63]
	s_add_u32 m0, s47, 0x0
	s_add_u32 s42, s42, 0x1800
	s_addc_u32 s43, s43, 0
	global_load_lds_dwordx4 v77, s[42:43]
	ds_read_b128 v[36:39], v84 offset:20480
	v_mfma_f32_32x32x16_f16 a[32:47], v[40:43], v[56:59], a[32:47]
	ds_read_b128 v[40:43], v84 offset:21504
	v_mfma_f32_32x32x16_f16 a[16:31], v[44:47], v[56:59], a[16:31]
	s_add_u32 m0, s48, 0x0
	s_add_u32 s44, s44, 0x1800
	s_addc_u32 s45, s45, 0
	global_load_lds_dwordx4 v78, s[44:45]
	ds_read_b128 v[44:47], v84 offset:22528
	v_mfma_f32_32x32x16_f16 a[0:15], v[48:51], v[56:59], a[0:15]
	ds_read_b128 v[48:51], v84 offset:23552
	s_waitcnt lgkmcnt(6)
	v_mfma_f32_32x32x16_f16 a[80:95], v[4:7], v[60:63], a[80:95]
	s_waitcnt vmcnt(24)
	ds_write_b128 v81, v[116:119]
	ds_write_b128 v81, v[120:123] offset:1024
	v_mfma_f32_32x32x16_f16 a[64:79], v[8:11], v[60:63], a[64:79]
	ds_write_b128 v81, v[124:127] offset:2048
	ds_write_b128 v81, v[128:131] offset:3072
	v_mfma_f32_32x32x16_f16 a[48:63], v[12:15], v[60:63], a[48:63]
	ds_read_b128 v[100:103], v95
	ds_read_b128 v[104:107], v96
	ds_read_b128 v[108:111], v97
	ds_read_b128 v[112:115], v94
	s_waitcnt vmcnt(10)
	s_waitcnt lgkmcnt(8)
	s_barrier
	ds_read_b128 v[4:7], v84 offset:54208
	ds_read_b128 v[8:11], v84 offset:55232
	ds_read_b128 v[12:15], v84 offset:56256
	v_mfma_f32_32x32x16_f16 a[32:47], v[16:19], v[60:63], a[32:47]
	ds_read_b128 v[16:19], v84 offset:57280
	v_mfma_f32_32x32x16_f16 a[16:31], v[20:23], v[60:63], a[16:31]
	ds_read_b128 v[20:23], v84 offset:58304
	v_mfma_f32_32x32x16_f16 a[0:15], v[24:27], v[60:63], a[0:15]
	ds_read_b128 v[24:27], v84 offset:59328
	s_waitcnt lgkmcnt(6)
	v_mfma_f32_32x32x16_f16 a[80:95], v[28:31], v[0:3], a[80:95]
	s_add_u32 m0, s46, 0x3000
	s_add_u32 s40, s40, 0x1800
	s_addc_u32 s41, s41, 0
	global_load_lds_dwordx4 v76, s[40:41]
	ds_read_b128 v[28:31], v84 offset:60352
	v_mfma_f32_32x32x16_f16 a[64:79], v[32:35], v[0:3], a[64:79]
	global_load_dwordx4 v[116:119], v64, s[4:5] offset:1440
	global_load_dwordx4 v[120:123], v66, s[4:5] offset:1440
	ds_read_b128 v[32:35], v84 offset:61376
	v_mfma_f32_32x32x16_f16 a[48:63], v[36:39], v[0:3], a[48:63]
	s_add_u32 m0, s47, 0x3000
	s_add_u32 s42, s42, 0x1800
	s_addc_u32 s43, s43, 0
	global_load_lds_dwordx4 v77, s[42:43]
	ds_read_b128 v[36:39], v84 offset:62400
	v_mfma_f32_32x32x16_f16 a[32:47], v[40:43], v[0:3], a[32:47]
	global_load_dwordx4 v[124:127], v68, s[4:5] offset:1440
	global_load_dwordx4 v[128:131], v70, s[4:5] offset:1440
	ds_read_b128 v[40:43], v84 offset:63424
	v_mfma_f32_32x32x16_f16 a[16:31], v[44:47], v[0:3], a[16:31]
	s_add_u32 m0, s48, 0x3000
	s_add_u32 s44, s44, 0x1800
	s_addc_u32 s45, s45, 0
	global_load_lds_dwordx4 v78, s[44:45]
	ds_read_b128 v[44:47], v84 offset:64448
	v_mfma_f32_32x32x16_f16 a[0:15], v[48:51], v[0:3], a[0:15]
	ds_read_b128 v[48:51], v84 offset:65472
	s_waitcnt lgkmcnt(6)
	v_mfma_f32_32x32x16_f16 a[80:95], v[4:7], v[100:103], a[80:95]
	v_mfma_f32_32x32x16_f16 a[64:79], v[8:11], v[100:103], a[64:79]
	v_mfma_f32_32x32x16_f16 a[48:63], v[12:15], v[100:103], a[48:63]
	s_waitcnt vmcnt(10)
	s_waitcnt lgkmcnt(0)
	s_barrier
	ds_read_b128 v[4:7], v98
	ds_read_b128 v[8:11], v98 offset:1024
	ds_read_b128 v[12:15], v98 offset:2048
	v_mfma_f32_32x32x16_f16 a[32:47], v[16:19], v[100:103], a[32:47]
	ds_read_b128 v[16:19], v98 offset:3072
	v_mfma_f32_32x32x16_f16 a[16:31], v[20:23], v[100:103], a[16:31]
	ds_read_b128 v[20:23], v98 offset:4096
	v_mfma_f32_32x32x16_f16 a[0:15], v[24:27], v[100:103], a[0:15]
	ds_read_b128 v[24:27], v98 offset:5120
	v_mfma_f32_32x32x16_f16 a[80:95], v[28:31], v[104:107], a[80:95]
	s_add_u32 m0, s46, 0xd3c0
	s_add_u32 s40, s40, 0x1800
	s_addc_u32 s41, s41, 0
	global_load_lds_dwordx4 v76, s[40:41]
	ds_read_b128 v[28:31], v98 offset:6144
	v_mfma_f32_32x32x16_f16 a[64:79], v[32:35], v[104:107], a[64:79]
	ds_read_b128 v[32:35], v98 offset:7168
	v_mfma_f32_32x32x16_f16 a[48:63], v[36:39], v[104:107], a[48:63]
	s_add_u32 m0, s47, 0xd3c0
	s_add_u32 s42, s42, 0x1800
	s_addc_u32 s43, s43, 0
	global_load_lds_dwordx4 v77, s[42:43]
	ds_read_b128 v[36:39], v98 offset:8192
	v_mfma_f32_32x32x16_f16 a[32:47], v[40:43], v[104:107], a[32:47]
	ds_read_b128 v[40:43], v98 offset:9216
	v_mfma_f32_32x32x16_f16 a[16:31], v[44:47], v[104:107], a[16:31]
	s_add_u32 m0, s48, 0xd3c0
	s_add_u32 s44, s44, 0x1800
	s_addc_u32 s45, s45, 0
	global_load_lds_dwordx4 v78, s[44:45]
	ds_read_b128 v[44:47], v98 offset:10240
	v_mfma_f32_32x32x16_f16 a[0:15], v[48:51], v[104:107], a[0:15]
	ds_read_b128 v[48:51], v98 offset:11264
	s_waitcnt lgkmcnt(6)
	v_mfma_f32_32x32x16_f16 a[80:95], v[4:7], v[108:111], a[80:95]
	s_waitcnt vmcnt(24)
	ds_write_b128 v81, v[132:135]
	ds_write_b128 v81, v[136:139] offset:1024
	v_mfma_f32_32x32x16_f16 a[64:79], v[8:11], v[108:111], a[64:79]
	ds_write_b128 v81, v[140:143] offset:2048
	ds_write_b128 v81, v[144:147] offset:3072
	v_mfma_f32_32x32x16_f16 a[48:63], v[12:15], v[108:111], a[48:63]
	ds_read_b128 v[52:55], v95
	ds_read_b128 v[56:59], v96
	ds_read_b128 v[60:63], v97
	ds_read_b128 v[0:3], v94
	s_waitcnt vmcnt(10)
	s_waitcnt lgkmcnt(8)
	s_barrier
	ds_read_b128 v[4:7], v84 offset:0
	ds_read_b128 v[8:11], v84 offset:1024
	ds_read_b128 v[12:15], v84 offset:2048
	v_mfma_f32_32x32x16_f16 a[32:47], v[16:19], v[108:111], a[32:47]
	ds_read_b128 v[16:19], v84 offset:3072
	v_mfma_f32_32x32x16_f16 a[16:31], v[20:23], v[108:111], a[16:31]
	ds_read_b128 v[20:23], v84 offset:4096
	v_mfma_f32_32x32x16_f16 a[0:15], v[24:27], v[108:111], a[0:15]
	ds_read_b128 v[24:27], v84 offset:5120
	s_waitcnt lgkmcnt(6)
	v_mfma_f32_32x32x16_f16 a[80:95], v[28:31], v[112:115], a[80:95]
	s_add_u32 m0, s46, 0x103c0
	s_add_u32 s40, s40, 0x1800
	s_addc_u32 s41, s41, 0
	global_load_lds_dwordx4 v76, s[40:41]
	ds_read_b128 v[28:31], v84 offset:6144
	v_mfma_f32_32x32x16_f16 a[64:79], v[32:35], v[112:115], a[64:79]
	ds_read_b128 v[32:35], v84 offset:7168
	v_mfma_f32_32x32x16_f16 a[48:63], v[36:39], v[112:115], a[48:63]
	s_add_u32 m0, s47, 0x103c0
	s_add_u32 s42, s42, 0x1800
	s_addc_u32 s43, s43, 0
	global_load_lds_dwordx4 v77, s[42:43]
	ds_read_b128 v[36:39], v84 offset:8192
	v_mfma_f32_32x32x16_f16 a[32:47], v[40:43], v[112:115], a[32:47]
	ds_read_b128 v[40:43], v84 offset:9216
	v_mfma_f32_32x32x16_f16 a[16:31], v[44:47], v[112:115], a[16:31]
	s_add_u32 m0, s48, 0x103c0
	s_add_u32 s44, s44, 0x1800
	s_addc_u32 s45, s45, 0
	global_load_lds_dwordx4 v78, s[44:45]
	ds_read_b128 v[44:47], v84 offset:10240
	v_mfma_f32_32x32x16_f16 a[0:15], v[48:51], v[112:115], a[0:15]
	ds_read_b128 v[48:51], v84 offset:11264
	s_waitcnt lgkmcnt(6)
	v_mfma_f32_32x32x16_f16 a[80:95], v[4:7], v[52:55], a[80:95]
	v_mfma_f32_32x32x16_f16 a[64:79], v[8:11], v[52:55], a[64:79]
	v_mfma_f32_32x32x16_f16 a[48:63], v[12:15], v[52:55], a[48:63]
	s_waitcnt vmcnt(6)
	s_waitcnt lgkmcnt(0)
	s_barrier
	ds_read_b128 v[4:7], v84 offset:12288
	ds_read_b128 v[8:11], v84 offset:13312
	ds_read_b128 v[12:15], v84 offset:14336
	v_mfma_f32_32x32x16_f16 a[32:47], v[16:19], v[52:55], a[32:47]
	ds_read_b128 v[16:19], v84 offset:15360
	v_mfma_f32_32x32x16_f16 a[16:31], v[20:23], v[52:55], a[16:31]
	ds_read_b128 v[20:23], v84 offset:16384
	v_mfma_f32_32x32x16_f16 a[0:15], v[24:27], v[52:55], a[0:15]
	ds_read_b128 v[24:27], v84 offset:17408
	v_mfma_f32_32x32x16_f16 a[80:95], v[28:31], v[56:59], a[80:95]
	s_add_u32 m0, s46, 0x0
	s_add_u32 s40, s40, 0x1800
	s_addc_u32 s41, s41, 0
	global_load_lds_dwordx4 v76, s[40:41]
	ds_read_b128 v[28:31], v84 offset:18432
	v_mfma_f32_32x32x16_f16 a[64:79], v[32:35], v[56:59], a[64:79]
	ds_read_b128 v[32:35], v84 offset:19456
	v_mfma_f32_32x32x16_f16 a[48:63], v[36:39], v[56:59], a[48:63]
	s_add_u32 m0, s47, 0x0
	s_add_u32 s42, s42, s49
	s_addc_u32 s43, s43, 0
	global_load_lds_dwordx4 v77, s[42:43]
	ds_read_b128 v[36:39], v84 offset:20480
	v_mfma_f32_32x32x16_f16 a[32:47], v[40:43], v[56:59], a[32:47]
	ds_read_b128 v[40:43], v84 offset:21504
	v_mfma_f32_32x32x16_f16 a[16:31], v[44:47], v[56:59], a[16:31]
	s_add_u32 m0, s48, 0x0
	s_add_u32 s44, s44, 0xc00
	s_addc_u32 s45, s45, 0
	global_load_lds_dwordx4 v78, s[44:45]
	ds_read_b128 v[44:47], v84 offset:22528
	v_mfma_f32_32x32x16_f16 a[0:15], v[48:51], v[56:59], a[0:15]
	ds_read_b128 v[48:51], v84 offset:23552
	s_waitcnt lgkmcnt(6)
	v_mfma_f32_32x32x16_f16 a[80:95], v[4:7], v[60:63], a[80:95]
	s_waitcnt vmcnt(20)
	ds_write_b128 v81, v[148:151]
	ds_write_b128 v81, v[152:155] offset:1024
	v_mfma_f32_32x32x16_f16 a[64:79], v[8:11], v[60:63], a[64:79]
	ds_write_b128 v81, v[156:159] offset:2048
	ds_write_b128 v81, v[72:75] offset:3072
	v_mfma_f32_32x32x16_f16 a[48:63], v[12:15], v[60:63], a[48:63]
	ds_read_b128 v[100:103], v95
	ds_read_b128 v[104:107], v96
	ds_read_b128 v[108:111], v97
	ds_read_b128 v[112:115], v94
	s_waitcnt vmcnt(6)
	s_waitcnt lgkmcnt(8)
	s_barrier
	ds_read_b128 v[4:7], v84 offset:54208
	ds_read_b128 v[8:11], v84 offset:55232
	ds_read_b128 v[12:15], v84 offset:56256
	v_mfma_f32_32x32x16_f16 a[32:47], v[16:19], v[60:63], a[32:47]
	ds_read_b128 v[16:19], v84 offset:57280
	v_mfma_f32_32x32x16_f16 a[16:31], v[20:23], v[60:63], a[16:31]
	ds_read_b128 v[20:23], v84 offset:58304
	v_mfma_f32_32x32x16_f16 a[0:15], v[24:27], v[60:63], a[0:15]
	ds_read_b128 v[24:27], v84 offset:59328
	s_waitcnt lgkmcnt(6)
	v_mfma_f32_32x32x16_f16 a[80:95], v[28:31], v[0:3], a[80:95]
	ds_read_b128 v[28:31], v84 offset:60352
	v_mfma_f32_32x32x16_f16 a[64:79], v[32:35], v[0:3], a[64:79]
	ds_read_b128 v[32:35], v84 offset:61376
	v_mfma_f32_32x32x16_f16 a[48:63], v[36:39], v[0:3], a[48:63]
	ds_read_b128 v[36:39], v84 offset:62400
	v_mfma_f32_32x32x16_f16 a[32:47], v[40:43], v[0:3], a[32:47]
	ds_read_b128 v[40:43], v84 offset:63424
	v_mfma_f32_32x32x16_f16 a[16:31], v[44:47], v[0:3], a[16:31]
	ds_read_b128 v[44:47], v84 offset:64448
	v_mfma_f32_32x32x16_f16 a[0:15], v[48:51], v[0:3], a[0:15]
	ds_read_b128 v[48:51], v84 offset:65472
	s_waitcnt lgkmcnt(6)
	v_mfma_f32_32x32x16_f16 a[80:95], v[4:7], v[100:103], a[80:95]
	v_mfma_f32_32x32x16_f16 a[64:79], v[8:11], v[100:103], a[64:79]
	v_mfma_f32_32x32x16_f16 a[48:63], v[12:15], v[100:103], a[48:63]
	s_waitcnt vmcnt(3)
	s_waitcnt lgkmcnt(0)
	s_barrier
	ds_read_b128 v[4:7], v98
	ds_read_b128 v[8:11], v98 offset:1024
	ds_read_b128 v[12:15], v98 offset:2048
	v_mfma_f32_32x32x16_f16 a[32:47], v[16:19], v[100:103], a[32:47]
	ds_read_b128 v[16:19], v98 offset:3072
	v_mfma_f32_32x32x16_f16 a[16:31], v[20:23], v[100:103], a[16:31]
	ds_read_b128 v[20:23], v98 offset:4096
	v_mfma_f32_32x32x16_f16 a[0:15], v[24:27], v[100:103], a[0:15]
	ds_read_b128 v[24:27], v98 offset:5120
	v_mfma_f32_32x32x16_f16 a[80:95], v[28:31], v[104:107], a[80:95]
	ds_read_b128 v[28:31], v98 offset:6144
	v_mfma_f32_32x32x16_f16 a[64:79], v[32:35], v[104:107], a[64:79]
	ds_read_b128 v[32:35], v98 offset:7168
	v_mfma_f32_32x32x16_f16 a[48:63], v[36:39], v[104:107], a[48:63]
	ds_read_b128 v[36:39], v98 offset:8192
	v_mfma_f32_32x32x16_f16 a[32:47], v[40:43], v[104:107], a[32:47]
	ds_read_b128 v[40:43], v98 offset:9216
	v_mfma_f32_32x32x16_f16 a[16:31], v[44:47], v[104:107], a[16:31]
	ds_read_b128 v[44:47], v98 offset:10240
	v_mfma_f32_32x32x16_f16 a[0:15], v[48:51], v[104:107], a[0:15]
	ds_read_b128 v[48:51], v98 offset:11264
	s_waitcnt lgkmcnt(6)
	v_mfma_f32_32x32x16_f16 a[80:95], v[4:7], v[108:111], a[80:95]
	s_waitcnt vmcnt(10)
	ds_write_b128 v81, v[116:119]
	ds_write_b128 v81, v[120:123] offset:1024
	v_mfma_f32_32x32x16_f16 a[64:79], v[8:11], v[108:111], a[64:79]
	ds_write_b128 v81, v[124:127] offset:2048
	ds_write_b128 v81, v[128:131] offset:3072
	v_mfma_f32_32x32x16_f16 a[48:63], v[12:15], v[108:111], a[48:63]
	ds_read_b128 v[0:3], v94
	s_waitcnt vmcnt(0)
	s_waitcnt lgkmcnt(5)
	s_barrier
	ds_read_b128 v[4:7], v84 offset:0
	ds_read_b128 v[8:11], v84 offset:1024
	ds_read_b128 v[12:15], v84 offset:2048
	v_mfma_f32_32x32x16_f16 a[32:47], v[16:19], v[108:111], a[32:47]
	ds_read_b128 v[16:19], v84 offset:3072
	v_mfma_f32_32x32x16_f16 a[16:31], v[20:23], v[108:111], a[16:31]
	ds_read_b128 v[20:23], v84 offset:4096
	v_mfma_f32_32x32x16_f16 a[0:15], v[24:27], v[108:111], a[0:15]
	ds_read_b128 v[24:27], v84 offset:5120
	s_waitcnt lgkmcnt(6)
	v_mfma_f32_32x32x16_f16 a[80:95], v[28:31], v[112:115], a[80:95]
	v_mfma_f32_32x32x16_f16 a[64:79], v[32:35], v[112:115], a[64:79]
	v_mfma_f32_32x32x16_f16 a[48:63], v[36:39], v[112:115], a[48:63]
	v_mfma_f32_32x32x16_f16 a[32:47], v[40:43], v[112:115], a[32:47]
	v_mfma_f32_32x32x16_f16 a[16:31], v[44:47], v[112:115], a[16:31]
	v_mfma_f32_32x32x16_f16 a[0:15], v[48:51], v[112:115], a[0:15]
	s_waitcnt lgkmcnt(0)
	v_mfma_f32_32x32x16_f16 a[80:95], v[4:7], v[0:3], a[80:95]
	v_mfma_f32_32x32x16_f16 a[16:31], v[20:23], v[0:3], a[16:31]
	v_lshlrev_b32_e32 v22, 4, v85
	v_mfma_f32_32x32x16_f16 a[64:79], v[8:11], v[0:3], a[64:79]
	v_mfma_f32_32x32x16_f16 a[48:63], v[12:15], v[0:3], a[48:63]
	s_nop 7
	v_accvgpr_read_b32 v13, a88
	v_mfma_f32_32x32x16_f16 a[32:47], v[16:19], v[0:3], a[32:47]
	v_accvgpr_read_b32 v17, a92
	v_mfma_f32_32x32x16_f16 a[0:15], v[24:27], v[0:3], a[0:15]
	ds_read_b128 v[2:5], v22 offset:53248
	ds_read_b128 v[6:9], v22 offset:53280
	v_accvgpr_read_b32 v1, a80
	v_lshlrev_b32_e32 v0, 4, v92
	s_waitcnt lgkmcnt(1)
	v_add_f32_e32 v1, v1, v2
	v_accvgpr_read_b32 v2, a81
	v_add_f32_e32 v2, v3, v2
	v_max_f32_e32 v10, 0, v2
	v_accvgpr_read_b32 v2, a82
	v_add_f32_e32 v2, v4, v2
	v_max_f32_e32 v11, 0, v2
	v_accvgpr_read_b32 v2, a83
	v_add_f32_e32 v2, v5, v2
	v_max_f32_e32 v12, 0, v2
	v_accvgpr_read_b32 v2, a84
	s_waitcnt lgkmcnt(0)
	v_add_f32_e32 v2, v2, v6
	v_max_f32_e32 v6, 0, v2
	v_accvgpr_read_b32 v2, a85
	v_add_f32_e32 v2, v7, v2
	v_max_f32_e32 v7, 0, v2
	v_accvgpr_read_b32 v2, a86
	v_add_f32_e32 v2, v8, v2
	v_max_f32_e32 v8, 0, v2
	v_accvgpr_read_b32 v2, a87
	v_add_f32_e32 v2, v9, v2
	v_max_f32_e32 v9, 0, v2
	ds_read_b128 v[2:5], v22 offset:53312
	v_max_f32_e32 v1, 0, v1
	s_waitcnt lgkmcnt(0)
	v_add_f32_e32 v2, v13, v2
	v_max_f32_e32 v13, 0, v2
	v_accvgpr_read_b32 v2, a89
	v_add_f32_e32 v2, v3, v2
	v_max_f32_e32 v14, 0, v2
	v_accvgpr_read_b32 v2, a90
	v_add_f32_e32 v2, v4, v2
	v_max_f32_e32 v15, 0, v2
	v_accvgpr_read_b32 v2, a91
	v_add_f32_e32 v2, v5, v2
	v_max_f32_e32 v16, 0, v2
	ds_read_b128 v[2:5], v22 offset:53344
	s_waitcnt lgkmcnt(0)
	v_add_f32_e32 v2, v17, v2
	v_max_f32_e32 v17, 0, v2
	v_accvgpr_read_b32 v2, a93
	v_add_f32_e32 v2, v3, v2
	v_max_f32_e32 v18, 0, v2
	v_accvgpr_read_b32 v2, a94
	v_add_f32_e32 v2, v4, v2
	v_max_f32_e32 v19, 0, v2
	v_accvgpr_read_b32 v2, a95
	v_add_f32_e32 v2, v5, v2
	v_cvt_pk_f16_f32 v5, v8, v9
	v_cvt_pk_f16_f32 v4, v6, v7
	ds_read_b128 v[6:9], v0 offset:40960
	v_max_f32_e32 v20, 0, v2
	v_cvt_pk_f16_f32 v3, v11, v12
	v_cvt_pk_f16_f32 v2, v1, v10
	v_accvgpr_read_b32 v1, a64
	s_waitcnt lgkmcnt(0)
	v_mfma_f32_32x32x16_f16 a[80:95], v[6:9], v[2:5], 0
	ds_read_b128 v[6:9], v0 offset:41984
	v_cvt_pk_f16_f32 v5, v19, v20
	v_cvt_pk_f16_f32 v4, v17, v18
	v_cvt_pk_f16_f32 v3, v15, v16
	v_cvt_pk_f16_f32 v2, v13, v14
	v_accvgpr_read_b32 v13, a72
	v_accvgpr_read_b32 v17, a76
	s_waitcnt lgkmcnt(0)
	v_mfma_f32_32x32x16_f16 a[80:95], v[6:9], v[2:5], a[80:95]
	ds_read_b128 v[2:5], v22 offset:53376
	v_accvgpr_read_b32 v9, a68
	s_waitcnt lgkmcnt(0)
	v_add_f32_e32 v1, v1, v2
	v_accvgpr_read_b32 v2, a65
	v_add_f32_e32 v2, v3, v2
	v_max_f32_e32 v6, 0, v2
	v_accvgpr_read_b32 v2, a66
	v_add_f32_e32 v2, v4, v2
	v_max_f32_e32 v7, 0, v2
	v_accvgpr_read_b32 v2, a67
	v_add_f32_e32 v2, v5, v2
	v_max_f32_e32 v8, 0, v2
	ds_read_b128 v[2:5], v22 offset:53408
	v_max_f32_e32 v1, 0, v1
	s_waitcnt lgkmcnt(0)
	v_add_f32_e32 v2, v9, v2
	v_max_f32_e32 v9, 0, v2
	v_accvgpr_read_b32 v2, a69
	v_add_f32_e32 v2, v3, v2
	v_max_f32_e32 v10, 0, v2
	v_accvgpr_read_b32 v2, a70
	v_add_f32_e32 v2, v4, v2
	v_max_f32_e32 v11, 0, v2
	v_accvgpr_read_b32 v2, a71
	v_add_f32_e32 v2, v5, v2
	v_max_f32_e32 v12, 0, v2
	ds_read_b128 v[2:5], v22 offset:53440
	s_waitcnt lgkmcnt(0)
	v_add_f32_e32 v2, v13, v2
	v_max_f32_e32 v13, 0, v2
	v_accvgpr_read_b32 v2, a73
	v_add_f32_e32 v2, v3, v2
	v_max_f32_e32 v14, 0, v2
	v_accvgpr_read_b32 v2, a74
	v_add_f32_e32 v2, v4, v2
	v_max_f32_e32 v15, 0, v2
	v_accvgpr_read_b32 v2, a75
	v_add_f32_e32 v2, v5, v2
	v_max_f32_e32 v16, 0, v2
	ds_read_b128 v[2:5], v22 offset:53472
	s_waitcnt lgkmcnt(0)
	v_add_f32_e32 v2, v17, v2
	v_max_f32_e32 v17, 0, v2
	v_accvgpr_read_b32 v2, a77
	v_add_f32_e32 v2, v3, v2
	v_max_f32_e32 v18, 0, v2
	v_accvgpr_read_b32 v2, a78
	v_add_f32_e32 v2, v4, v2
	v_max_f32_e32 v19, 0, v2
	v_accvgpr_read_b32 v2, a79
	v_add_f32_e32 v2, v5, v2
	v_max_f32_e32 v20, 0, v2
	v_cvt_pk_f16_f32 v4, v9, v10
	v_cvt_pk_f16_f32 v3, v7, v8
	v_cvt_pk_f16_f32 v2, v1, v6
	ds_read_b128 v[6:9], v0 offset:43008
	v_cvt_pk_f16_f32 v5, v11, v12
	v_accvgpr_read_b32 v1, a48
	s_waitcnt lgkmcnt(0)
	v_mfma_f32_32x32x16_f16 a[80:95], v[6:9], v[2:5], a[80:95]
	ds_read_b128 v[6:9], v0 offset:44032
	v_cvt_pk_f16_f32 v5, v19, v20
	v_cvt_pk_f16_f32 v4, v17, v18
	v_cvt_pk_f16_f32 v3, v15, v16
	v_cvt_pk_f16_f32 v2, v13, v14
	v_accvgpr_read_b32 v13, a56
	v_accvgpr_read_b32 v17, a60
	s_waitcnt lgkmcnt(0)
	v_mfma_f32_32x32x16_f16 a[80:95], v[6:9], v[2:5], a[80:95]
	ds_read_b128 v[2:5], v22 offset:53504
	v_accvgpr_read_b32 v9, a52
	s_waitcnt lgkmcnt(0)
	v_add_f32_e32 v1, v1, v2
	v_accvgpr_read_b32 v2, a49
	v_add_f32_e32 v2, v3, v2
	v_max_f32_e32 v6, 0, v2
	v_accvgpr_read_b32 v2, a50
	v_add_f32_e32 v2, v4, v2
	v_max_f32_e32 v7, 0, v2
	v_accvgpr_read_b32 v2, a51
	v_add_f32_e32 v2, v5, v2
	v_max_f32_e32 v8, 0, v2
	ds_read_b128 v[2:5], v22 offset:53536
	v_max_f32_e32 v1, 0, v1
	s_waitcnt lgkmcnt(0)
	v_add_f32_e32 v2, v9, v2
	v_max_f32_e32 v9, 0, v2
	v_accvgpr_read_b32 v2, a53
	v_add_f32_e32 v2, v3, v2
	v_max_f32_e32 v10, 0, v2
	v_accvgpr_read_b32 v2, a54
	v_add_f32_e32 v2, v4, v2
	v_max_f32_e32 v11, 0, v2
	v_accvgpr_read_b32 v2, a55
	v_add_f32_e32 v2, v5, v2
	v_max_f32_e32 v12, 0, v2
	ds_read_b128 v[2:5], v22 offset:53568
	s_waitcnt lgkmcnt(0)
	v_add_f32_e32 v2, v13, v2
	v_max_f32_e32 v13, 0, v2
	v_accvgpr_read_b32 v2, a57
	v_add_f32_e32 v2, v3, v2
	v_max_f32_e32 v14, 0, v2
	v_accvgpr_read_b32 v2, a58
	v_add_f32_e32 v2, v4, v2
	v_max_f32_e32 v15, 0, v2
	v_accvgpr_read_b32 v2, a59
	v_add_f32_e32 v2, v5, v2
	v_max_f32_e32 v16, 0, v2
	ds_read_b128 v[2:5], v22 offset:53600
	s_waitcnt lgkmcnt(0)
	v_add_f32_e32 v2, v17, v2
	v_max_f32_e32 v17, 0, v2
	v_accvgpr_read_b32 v2, a61
	v_add_f32_e32 v2, v3, v2
	v_max_f32_e32 v18, 0, v2
	v_accvgpr_read_b32 v2, a62
	v_add_f32_e32 v2, v4, v2
	v_max_f32_e32 v19, 0, v2
	v_accvgpr_read_b32 v2, a63
	v_add_f32_e32 v2, v5, v2
	v_max_f32_e32 v20, 0, v2
	v_cvt_pk_f16_f32 v4, v9, v10
	v_cvt_pk_f16_f32 v3, v7, v8
	v_cvt_pk_f16_f32 v2, v1, v6
	ds_read_b128 v[6:9], v0 offset:45056
	v_cvt_pk_f16_f32 v5, v11, v12
	v_accvgpr_read_b32 v1, a32
	s_waitcnt lgkmcnt(0)
	v_mfma_f32_32x32x16_f16 a[80:95], v[6:9], v[2:5], a[80:95]
	ds_read_b128 v[6:9], v0 offset:46080
	v_cvt_pk_f16_f32 v5, v19, v20
	v_cvt_pk_f16_f32 v4, v17, v18
	v_cvt_pk_f16_f32 v3, v15, v16
	v_cvt_pk_f16_f32 v2, v13, v14
	v_accvgpr_read_b32 v13, a40
	v_accvgpr_read_b32 v17, a44
	s_waitcnt lgkmcnt(0)
	v_mfma_f32_32x32x16_f16 a[80:95], v[6:9], v[2:5], a[80:95]
	ds_read_b128 v[2:5], v22 offset:53632
	v_accvgpr_read_b32 v9, a36
	s_waitcnt lgkmcnt(0)
	v_add_f32_e32 v1, v1, v2
	v_accvgpr_read_b32 v2, a33
	v_add_f32_e32 v2, v3, v2
	v_max_f32_e32 v6, 0, v2
	v_accvgpr_read_b32 v2, a34
	v_add_f32_e32 v2, v4, v2
	v_max_f32_e32 v7, 0, v2
	v_accvgpr_read_b32 v2, a35
	v_add_f32_e32 v2, v5, v2
	v_max_f32_e32 v8, 0, v2
	ds_read_b128 v[2:5], v22 offset:53664
	v_max_f32_e32 v1, 0, v1
	s_waitcnt lgkmcnt(0)
	v_add_f32_e32 v2, v9, v2
	v_max_f32_e32 v9, 0, v2
	v_accvgpr_read_b32 v2, a37
	v_add_f32_e32 v2, v3, v2
	v_max_f32_e32 v10, 0, v2
	v_accvgpr_read_b32 v2, a38
	v_add_f32_e32 v2, v4, v2
	v_max_f32_e32 v11, 0, v2
	v_accvgpr_read_b32 v2, a39
	v_add_f32_e32 v2, v5, v2
	v_max_f32_e32 v12, 0, v2
	ds_read_b128 v[2:5], v22 offset:53696
	s_waitcnt lgkmcnt(0)
	v_add_f32_e32 v2, v13, v2
	v_max_f32_e32 v13, 0, v2
	v_accvgpr_read_b32 v2, a41
	v_add_f32_e32 v2, v3, v2
	v_max_f32_e32 v14, 0, v2
	v_accvgpr_read_b32 v2, a42
	v_add_f32_e32 v2, v4, v2
	v_max_f32_e32 v15, 0, v2
	v_accvgpr_read_b32 v2, a43
	v_add_f32_e32 v2, v5, v2
	v_max_f32_e32 v16, 0, v2
	ds_read_b128 v[2:5], v22 offset:53728
	s_waitcnt lgkmcnt(0)
	v_add_f32_e32 v2, v17, v2
	v_max_f32_e32 v17, 0, v2
	v_accvgpr_read_b32 v2, a45
	v_add_f32_e32 v2, v3, v2
	v_max_f32_e32 v18, 0, v2
	v_accvgpr_read_b32 v2, a46
	v_add_f32_e32 v2, v4, v2
	v_max_f32_e32 v19, 0, v2
	v_accvgpr_read_b32 v2, a47
	v_add_f32_e32 v2, v5, v2
	v_max_f32_e32 v20, 0, v2
	v_cvt_pk_f16_f32 v4, v9, v10
	v_cvt_pk_f16_f32 v3, v7, v8
	v_cvt_pk_f16_f32 v2, v1, v6
	ds_read_b128 v[6:9], v0 offset:47104
	v_cvt_pk_f16_f32 v5, v11, v12
	v_accvgpr_read_b32 v1, a16
	s_waitcnt lgkmcnt(0)
	v_mfma_f32_32x32x16_f16 a[32:47], v[6:9], v[2:5], 0
	ds_read_b128 v[6:9], v0 offset:48128
	v_cvt_pk_f16_f32 v5, v19, v20
	v_cvt_pk_f16_f32 v4, v17, v18
	v_cvt_pk_f16_f32 v3, v15, v16
	v_cvt_pk_f16_f32 v2, v13, v14
	v_accvgpr_read_b32 v13, a24
	v_accvgpr_read_b32 v17, a28
	s_waitcnt lgkmcnt(0)
	v_mfma_f32_32x32x16_f16 a[32:47], v[6:9], v[2:5], a[32:47]
	ds_read_b128 v[2:5], v22 offset:53760
	v_accvgpr_read_b32 v9, a20
	s_waitcnt lgkmcnt(0)
	v_add_f32_e32 v1, v1, v2
	v_accvgpr_read_b32 v2, a17
	v_add_f32_e32 v2, v3, v2
	v_max_f32_e32 v6, 0, v2
	v_accvgpr_read_b32 v2, a18
	v_add_f32_e32 v2, v4, v2
	v_max_f32_e32 v7, 0, v2
	v_accvgpr_read_b32 v2, a19
	v_add_f32_e32 v2, v5, v2
	v_max_f32_e32 v8, 0, v2
	ds_read_b128 v[2:5], v22 offset:53792
	v_max_f32_e32 v1, 0, v1
	s_waitcnt lgkmcnt(0)
	v_add_f32_e32 v2, v9, v2
	v_max_f32_e32 v9, 0, v2
	v_accvgpr_read_b32 v2, a21
	v_add_f32_e32 v2, v3, v2
	v_max_f32_e32 v10, 0, v2
	v_accvgpr_read_b32 v2, a22
	v_add_f32_e32 v2, v4, v2
	v_max_f32_e32 v11, 0, v2
	v_accvgpr_read_b32 v2, a23
	v_add_f32_e32 v2, v5, v2
	v_max_f32_e32 v12, 0, v2
	ds_read_b128 v[2:5], v22 offset:53824
	s_waitcnt lgkmcnt(0)
	v_add_f32_e32 v2, v13, v2
	v_max_f32_e32 v13, 0, v2
	v_accvgpr_read_b32 v2, a25
	v_add_f32_e32 v2, v3, v2
	v_max_f32_e32 v14, 0, v2
	v_accvgpr_read_b32 v2, a26
	v_add_f32_e32 v2, v4, v2
	v_max_f32_e32 v15, 0, v2
	v_accvgpr_read_b32 v2, a27
	v_add_f32_e32 v2, v5, v2
	v_max_f32_e32 v16, 0, v2
	ds_read_b128 v[2:5], v22 offset:53856
	s_waitcnt lgkmcnt(0)
	v_add_f32_e32 v2, v17, v2
	v_max_f32_e32 v17, 0, v2
	v_accvgpr_read_b32 v2, a29
	v_add_f32_e32 v2, v3, v2
	v_max_f32_e32 v18, 0, v2
	v_accvgpr_read_b32 v2, a30
	v_add_f32_e32 v2, v4, v2
	v_max_f32_e32 v19, 0, v2
	v_accvgpr_read_b32 v2, a31
	v_add_f32_e32 v2, v5, v2
	v_max_f32_e32 v20, 0, v2
	v_cvt_pk_f16_f32 v4, v9, v10
	v_cvt_pk_f16_f32 v3, v7, v8
	v_cvt_pk_f16_f32 v2, v1, v6
	ds_read_b128 v[6:9], v0 offset:49152
	v_cvt_pk_f16_f32 v5, v11, v12
	v_accvgpr_read_b32 v1, a0
	s_waitcnt lgkmcnt(0)
	v_mfma_f32_32x32x16_f16 a[32:47], v[6:9], v[2:5], a[32:47]
	ds_read_b128 v[6:9], v0 offset:50176
	v_cvt_pk_f16_f32 v5, v19, v20
	v_cvt_pk_f16_f32 v4, v17, v18
	v_cvt_pk_f16_f32 v3, v15, v16
	v_cvt_pk_f16_f32 v2, v13, v14
	v_accvgpr_read_b32 v13, a8
	v_accvgpr_read_b32 v17, a12
	s_waitcnt lgkmcnt(0)
	v_mfma_f32_32x32x16_f16 a[32:47], v[6:9], v[2:5], a[32:47]
	ds_read_b128 v[2:5], v22 offset:53888
	v_accvgpr_read_b32 v9, a4
	s_waitcnt lgkmcnt(0)
	v_add_f32_e32 v1, v1, v2
	v_accvgpr_read_b32 v2, a1
	v_add_f32_e32 v2, v3, v2
	v_max_f32_e32 v6, 0, v2
	v_accvgpr_read_b32 v2, a2
	v_add_f32_e32 v2, v4, v2
	v_max_f32_e32 v7, 0, v2
	v_accvgpr_read_b32 v2, a3
	v_add_f32_e32 v2, v5, v2
	v_max_f32_e32 v8, 0, v2
	ds_read_b128 v[2:5], v22 offset:53920
	v_max_f32_e32 v1, 0, v1
	s_waitcnt lgkmcnt(0)
	v_add_f32_e32 v2, v9, v2
	v_max_f32_e32 v9, 0, v2
	v_accvgpr_read_b32 v2, a5
	v_add_f32_e32 v2, v3, v2
	v_max_f32_e32 v10, 0, v2
	v_accvgpr_read_b32 v2, a6
	v_add_f32_e32 v2, v4, v2
	v_max_f32_e32 v11, 0, v2
	v_accvgpr_read_b32 v2, a7
	v_add_f32_e32 v2, v5, v2
	v_max_f32_e32 v12, 0, v2
	ds_read_b128 v[2:5], v22 offset:53952
	s_waitcnt lgkmcnt(0)
	v_add_f32_e32 v2, v13, v2
	v_max_f32_e32 v13, 0, v2
	v_accvgpr_read_b32 v2, a9
	v_add_f32_e32 v2, v3, v2
	v_max_f32_e32 v14, 0, v2
	v_accvgpr_read_b32 v2, a10
	v_add_f32_e32 v2, v4, v2
	v_max_f32_e32 v15, 0, v2
	v_accvgpr_read_b32 v2, a11
	v_add_f32_e32 v2, v5, v2
	v_max_f32_e32 v16, 0, v2
	ds_read_b128 v[2:5], v22 offset:53984
	s_waitcnt lgkmcnt(0)
	v_add_f32_e32 v2, v17, v2
	v_max_f32_e32 v17, 0, v2
	v_accvgpr_read_b32 v2, a13
	v_add_f32_e32 v2, v3, v2
	v_max_f32_e32 v18, 0, v2
	v_accvgpr_read_b32 v2, a14
	v_add_f32_e32 v2, v4, v2
	v_max_f32_e32 v19, 0, v2
	v_accvgpr_read_b32 v2, a15
	v_add_f32_e32 v2, v5, v2
	v_max_f32_e32 v20, 0, v2
	v_cvt_pk_f16_f32 v4, v9, v10
	v_cvt_pk_f16_f32 v3, v7, v8
	v_cvt_pk_f16_f32 v2, v1, v6
	ds_read_b128 v[6:9], v0 offset:51200
	v_cvt_pk_f16_f32 v5, v11, v12
	s_waitcnt lgkmcnt(0)
	s_nop 0
	v_mfma_f32_32x32x16_f16 a[32:47], v[6:9], v[2:5], a[32:47]
	ds_read_b128 v[6:9], v0 offset:52224
	v_cvt_pk_f16_f32 v5, v19, v20
	v_cvt_pk_f16_f32 v4, v17, v18
	v_cvt_pk_f16_f32 v3, v15, v16
	v_cvt_pk_f16_f32 v2, v13, v14
	s_waitcnt lgkmcnt(0)
	s_nop 0
	v_mfma_f32_32x32x16_f16 a[32:47], v[6:9], v[2:5], a[32:47]
	s_and_saveexec_b64 s[2:3], s[0:1]
	s_cbranch_execz .LBB3_39
	v_accvgpr_read_b32 v0, a80
	v_accvgpr_read_b32 v6, a86
	v_accvgpr_read_b32 v7, a87
	v_accvgpr_read_b32 v8, a88
	v_accvgpr_read_b32 v9, a89
	v_accvgpr_read_b32 v10, a90
	v_accvgpr_read_b32 v11, a91
	v_accvgpr_read_b32 v12, a92
	v_accvgpr_read_b32 v13, a93
	v_accvgpr_read_b32 v14, a94
	v_accvgpr_read_b32 v15, a95
	v_accvgpr_read_b32 v6, a32
	v_accvgpr_read_b32 v14, a40
	v_accvgpr_read_b32 v15, a41
	v_accvgpr_read_b32 v16, a42
	v_accvgpr_read_b32 v17, a43
	v_accvgpr_read_b32 v18, a44
	v_accvgpr_read_b32 v19, a45
	v_accvgpr_read_b32 v20, a46
	v_accvgpr_read_b32 v21, a47
	ds_read_b128 v[14:17], v22 offset:54016
	ds_read_b128 v[18:21], v22 offset:54080
	v_accvgpr_read_b32 v12, a38
	v_accvgpr_read_b32 v13, a39
	v_lshlrev_b32_e32 v24, 2, v85
	v_accvgpr_read_b32 v1, a81
	v_accvgpr_read_b32 v7, a33
	v_mad_i64_i32 v[12:13], s[0:1], v80, 40, s[18:19]
	v_ashrrev_i32_e32 v25, 31, v24
	v_accvgpr_read_b32 v3, a83
	v_accvgpr_read_b32 v9, a35
	v_lshl_add_u64 v[22:23], v[24:25], 2, v[12:13]
	v_mov_b32_e32 v25, v1
	s_waitcnt lgkmcnt(1)
	v_mov_b32_e32 v27, v15
	v_mov_b32_e32 v1, v7
	s_waitcnt lgkmcnt(0)
	v_mov_b32_e32 v15, v19
	v_accvgpr_read_b32 v2, a82
	v_accvgpr_read_b32 v8, a34
	v_pk_add_f32 v[0:1], v[0:1], v[14:15]
	v_mov_b32_e32 v7, v3
	v_mov_b32_e32 v15, v17
	v_mov_b32_e32 v3, v9
	v_mov_b32_e32 v17, v21
	v_mov_b32_e32 v24, v6
	v_mov_b32_e32 v26, v18
	v_mov_b32_e32 v6, v8
	v_mov_b32_e32 v14, v20
	v_pk_add_f32 v[2:3], v[2:3], v[16:17]
	v_pk_add_f32 v[24:25], v[24:25], v[26:27]
	s_waitcnt vmcnt(0)
	v_pk_mul_f32 v[0:1], v[82:83], v[0:1]
	v_pk_add_f32 v[6:7], v[6:7], v[14:15]
	v_pk_mul_f32 v[2:3], v[82:83], v[2:3]
	v_accvgpr_read_b32 v4, a84
	v_accvgpr_read_b32 v5, a85
	v_accvgpr_read_b32 v10, a36
	v_accvgpr_read_b32 v11, a37
	v_pk_fma_f32 v[0:1], v[82:83], v[24:25], v[0:1] op_sel:[1,0,0] op_sel_hi:[0,1,1]
	v_pk_fma_f32 v[2:3], v[82:83], v[6:7], v[2:3] op_sel:[1,0,0] op_sel_hi:[0,1,1]
	v_cmp_eq_u32_e32 vcc, 0, v85
	global_store_dwordx4 v[22:23], v[0:3], off
	s_and_b64 exec, exec, vcc
	s_cbranch_execz .LBB3_39
	s_mov_b32 s0, 0xd000
	v_add_u32_e64 v0, s0, 0
	ds_read2_b64 v[0:3], v0 offset0:100 offset1:108
	v_mov_b32_e32 v9, v5
	v_mov_b32_e32 v5, v11
	v_mov_b32_e32 v8, v10
	v_pk_mov_b32 v[6:7], v[82:83], v[82:83] op_sel:[1,0]
	s_waitcnt lgkmcnt(0)
	v_mov_b32_e32 v15, v1
	v_mov_b32_e32 v1, v3
	v_mov_b32_e32 v14, v2
	v_pk_add_f32 v[0:1], v[4:5], v[0:1]
	v_pk_add_f32 v[8:9], v[8:9], v[14:15]
	v_pk_mul_f32 v[0:1], v[82:83], v[0:1]
	s_nop 0
	v_pk_fma_f32 v[0:1], v[6:7], v[8:9], v[0:1]
	global_store_dwordx2 v[12:13], v[0:1], off offset:32
